# v70 + SGU normalise steps: pairs of channels converted with one v_cvt_pk_bf16_f32 and written with ds_write_b16 + ds_write_b16_d16_hi (64 fewer VALU per unit)
# baseline (speedup 1.0000x reference)
.LBB0_488:
	s_or_b64 exec, exec, s[20:21]
	s_lshl_b64 s[4:5], s[52:53], 2
	s_add_u32 s13, s18, s4
	s_addc_u32 s21, s19, s5
	v_readlane_b32 s4, v255, 23
	v_readlane_b32 s5, v255, 24
	s_lshl_b64 s[4:5], s[4:5], 2
	s_add_u32 s16, s16, s4
	s_addc_u32 s17, s17, s5
	s_add_u32 s18, s10, 0x27c20000
	s_mul_i32 s4, s12, 0x4400
	s_addc_u32 s19, s11, 0
	s_add_i32 s20, s4, 0
	s_lshl_b64 s[4:5], s[6:7], 2
	v_lshlrev_b32_e32 v2, 3, v144
	s_add_u32 s4, s13, s4
	s_addc_u32 s5, s21, s5
	v_lshlrev_b32_e32 v6, 2, v2
	s_waitcnt lgkmcnt(0)
	s_barrier
	global_load_dwordx4 v[2:5], v6, s[4:5] offset:16
	s_nop 0
	global_load_dwordx4 v[6:9], v6, s[4:5]
	s_add_i32 s7, 0, 0x22000
	v_lshl_add_u32 v161, v0, 5, s7
	ds_read_b128 v[162:165], v161
	ds_read_b128 v[166:169], v161 offset:16
	v_and_b32_e32 v103, 63, v87
	v_and_b32_e32 v105, 31, v87
	v_or_b32_e32 v160, 8, v0
	s_waitcnt lgkmcnt(1)
	v_add_f32_e32 v161, v162, v163
	v_add_f32_e32 v162, v164, v165
	v_add_f32_e32 v161, v161, v162
	s_waitcnt lgkmcnt(0)
	v_add_f32_e32 v162, v166, v167
	v_add_f32_e32 v161, v161, v162
	v_add_f32_e32 v162, v168, v169
	v_add_f32_e32 v161, v162, v161
	v_fmamk_f32 v161, v161, 0x3b000000, v235
	v_rsq_f32_e32 v161, v161
	v_or_b32_e32 v159, 16, v0
	v_or_b32_e32 v150, 24, v0
	v_or_b32_e32 v149, 32, v0
	v_mul_f32_e32 v151, v161, v151
	v_or_b32_e32 v148, 40, v0
	v_or_b32_e32 v147, 48, v0
	v_or_b32_e32 v146, 56, v0
	v_or_b32_e32 v145, 64, v0
	v_or_b32_e32 v143, 0x48, v0
	v_or_b32_e32 v134, 0x50, v0
	v_or_b32_e32 v133, 0x58, v0
	v_or_b32_e32 v132, 0x60, v0
	v_or_b32_e32 v128, 0x68, v0
	v_or_b32_e32 v87, 0x70, v0
	v_or_b32_e32 v49, 0x78, v0
	v_mul_f32_e32 v152, v161, v152
	v_mul_f32_e32 v154, v161, v154
	v_mul_f32_e32 v153, v161, v153
	v_mul_f32_e32 v156, v161, v156
	v_mul_f32_e32 v155, v161, v155
	v_mul_f32_e32 v158, v161, v158
	v_mul_f32_e32 v157, v161, v157
	v_lshlrev_b32_e32 v161, 1, v0
	v_mul_u32_u24_e32 v0, 0x880, v144
	v_lshrrev_b32_e32 v144, 1, v144
	v_lshl_add_u32 v161, v144, 4, v161
	v_add3_u32 v144, s20, v161, v0
	s_ashr_i32 s13, s12, 31
	s_lshl_b64 s[4:5], s[12:13], 15
	v_lshrrev_b32_e32 v106, 5, v103
	s_add_u32 s4, s10, s4
	s_addc_u32 s5, s11, s5
	s_lshl_b32 s23, s12, 4
	s_waitcnt vmcnt(1)
	v_mul_f32_e32 v156, v2, v156
	s_waitcnt vmcnt(0)
	v_mul_f32_e32 v151, v7, v151
	v_mul_f32_e32 v154, v8, v154
	v_mul_f32_e32 v153, v9, v153
	v_cvt_pk_bf16_f32 v151, v151, v154
	ds_write_b16 v144, v151 offset:272
	ds_write_b16_d16_hi v144, v151 offset:544
	v_mul_f32_e32 v155, v3, v155
	v_mul_f32_e32 v158, v4, v158
	v_cvt_pk_bf16_f32 v151, v153, v156
	ds_write_b16 v144, v151 offset:816
	ds_write_b16_d16_hi v144, v151 offset:1088
	v_mul_f32_e32 v152, v6, v152
	v_mul_f32_e32 v157, v5, v157
	v_cvt_pk_bf16_f32 v151, v155, v158
	ds_write_b16 v144, v151 offset:1360
	ds_write_b16_d16_hi v144, v151 offset:1632
	v_cvt_pk_bf16_f32 v151, v152, v157
	ds_write_b16 v144, v151
	ds_write_b16_d16_hi v144, v151 offset:1904
	v_lshl_add_u32 v144, v160, 5, s7
	ds_read_b128 v[152:155], v144
	ds_read_b128 v[162:165], v144 offset:16
	s_waitcnt lgkmcnt(1)
	v_add_f32_e32 v144, v152, v153
	v_add_f32_e32 v151, v154, v155
	v_add_f32_e32 v144, v144, v151
	s_waitcnt lgkmcnt(0)
	v_add_f32_e32 v151, v162, v163
	v_add_f32_e32 v144, v144, v151
	v_add_f32_e32 v151, v164, v165
	v_add_f32_e32 v144, v151, v144
	v_fmamk_f32 v144, v144, 0x3b000000, v235
	v_rsq_f32_e32 v144, v144
	s_nop 0
	v_mul_f32_e32 v135, v144, v135
	v_mul_f32_e32 v136, v144, v136
	v_mul_f32_e32 v135, v7, v135
	v_mul_f32_e32 v138, v144, v138
	v_mul_f32_e32 v137, v144, v137
	v_mul_f32_e32 v140, v144, v140
	v_mul_f32_e32 v139, v144, v139
	v_mul_f32_e32 v142, v144, v142
	v_mul_f32_e32 v141, v144, v141
	v_bfe_u32 v144, v0, 8, 2
	v_lshlrev_b32_e32 v144, 3, v144
	v_xor_b32_e32 v144, v144, v160
	v_lshlrev_b32_e32 v144, 1, v144
	v_mul_f32_e32 v138, v8, v138
	v_add3_u32 v144, s20, v144, v0
	v_mul_f32_e32 v137, v9, v137
	v_mul_f32_e32 v140, v2, v140
	v_cvt_pk_bf16_f32 v135, v135, v138
	ds_write_b16 v144, v135 offset:272
	ds_write_b16_d16_hi v144, v135 offset:544
	v_mul_f32_e32 v139, v3, v139
	v_mul_f32_e32 v142, v4, v142
	v_cvt_pk_bf16_f32 v135, v137, v140
	ds_write_b16 v144, v135 offset:816
	ds_write_b16_d16_hi v144, v135 offset:1088
	v_mul_f32_e32 v136, v6, v136
	v_mul_f32_e32 v141, v5, v141
	v_cvt_pk_bf16_f32 v135, v139, v142
	ds_write_b16 v144, v135 offset:1360
	ds_write_b16_d16_hi v144, v135 offset:1632
	v_cvt_pk_bf16_f32 v135, v136, v141
	ds_write_b16 v144, v135
	ds_write_b16_d16_hi v144, v135 offset:1904
	v_lshl_add_u32 v135, v159, 5, s7
	ds_read_b128 v[136:139], v135
	ds_read_b128 v[152:155], v135 offset:16
	s_waitcnt lgkmcnt(1)
	v_add_f32_e32 v135, v136, v137
	v_add_f32_e32 v136, v138, v139
	v_add_f32_e32 v135, v135, v136
	s_waitcnt lgkmcnt(0)
	v_add_f32_e32 v136, v152, v153
	v_add_f32_e32 v135, v135, v136
	v_add_f32_e32 v136, v154, v155
	v_add_f32_e32 v135, v136, v135
	v_fmamk_f32 v135, v135, 0x3b000000, v235
	v_rsq_f32_e32 v135, v135
	s_nop 0
	v_mul_f32_e32 v123, v135, v123
	v_mul_f32_e32 v124, v135, v124
	v_mul_f32_e32 v123, v7, v123
	v_mul_f32_e32 v126, v135, v126
	v_mul_f32_e32 v125, v135, v125
	v_mul_f32_e32 v129, v135, v129
	v_mul_f32_e32 v127, v135, v127
	v_mul_f32_e32 v131, v135, v131
	v_mul_f32_e32 v130, v135, v130
	v_bfe_u32 v135, v0, 8, 2
	v_lshlrev_b32_e32 v135, 3, v135
	v_xor_b32_e32 v135, v135, v159
	v_lshlrev_b32_e32 v135, 1, v135
	v_mul_f32_e32 v126, v8, v126
	v_add3_u32 v135, s20, v135, v0
	v_mul_f32_e32 v125, v9, v125
	v_mul_f32_e32 v129, v2, v129
	v_cvt_pk_bf16_f32 v123, v123, v126
	ds_write_b16 v135, v123 offset:272
	ds_write_b16_d16_hi v135, v123 offset:544
	v_mul_f32_e32 v127, v3, v127
	v_mul_f32_e32 v131, v4, v131
	v_cvt_pk_bf16_f32 v123, v125, v129
	ds_write_b16 v135, v123 offset:816
	ds_write_b16_d16_hi v135, v123 offset:1088
	v_mul_f32_e32 v124, v6, v124
	v_mul_f32_e32 v130, v5, v130
	v_cvt_pk_bf16_f32 v123, v127, v131
	ds_write_b16 v135, v123 offset:1360
	ds_write_b16_d16_hi v135, v123 offset:1632
	v_cvt_pk_bf16_f32 v123, v124, v130
	ds_write_b16 v135, v123
	ds_write_b16_d16_hi v135, v123 offset:1904
	v_lshl_add_u32 v123, v150, 5, s7
	ds_read_b128 v[124:127], v123
	ds_read_b128 v[136:139], v123 offset:16
	s_waitcnt lgkmcnt(1)
	v_add_f32_e32 v123, v124, v125
	v_add_f32_e32 v124, v126, v127
	v_add_f32_e32 v123, v123, v124
	s_waitcnt lgkmcnt(0)
	v_add_f32_e32 v124, v136, v137
	v_add_f32_e32 v123, v123, v124
	v_add_f32_e32 v124, v138, v139
	v_add_f32_e32 v123, v124, v123
	v_fmamk_f32 v123, v123, 0x3b000000, v235
	v_rsq_f32_e32 v123, v123
	s_nop 0
	v_mul_f32_e32 v115, v123, v115
	v_mul_f32_e32 v116, v123, v116
	v_mul_f32_e32 v115, v7, v115
	v_mul_f32_e32 v118, v123, v118
	v_mul_f32_e32 v117, v123, v117
	v_mul_f32_e32 v120, v123, v120
	v_mul_f32_e32 v119, v123, v119
	v_mul_f32_e32 v122, v123, v122
	v_mul_f32_e32 v121, v123, v121
	v_bfe_u32 v123, v0, 8, 2
	v_lshlrev_b32_e32 v123, 3, v123
	v_xor_b32_e32 v123, v123, v150
	v_lshlrev_b32_e32 v123, 1, v123
	v_mul_f32_e32 v118, v8, v118
	v_add3_u32 v123, s20, v123, v0
	v_mul_f32_e32 v117, v9, v117
	v_mul_f32_e32 v120, v2, v120
	v_cvt_pk_bf16_f32 v115, v115, v118
	ds_write_b16 v123, v115 offset:272
	ds_write_b16_d16_hi v123, v115 offset:544
	v_mul_f32_e32 v119, v3, v119
	v_mul_f32_e32 v122, v4, v122
	v_cvt_pk_bf16_f32 v115, v117, v120
	ds_write_b16 v123, v115 offset:816
	ds_write_b16_d16_hi v123, v115 offset:1088
	v_mul_f32_e32 v116, v6, v116
	v_mul_f32_e32 v121, v5, v121
	v_cvt_pk_bf16_f32 v115, v119, v122
	ds_write_b16 v123, v115 offset:1360
	ds_write_b16_d16_hi v123, v115 offset:1632
	v_cvt_pk_bf16_f32 v115, v116, v121
	ds_write_b16 v123, v115
	ds_write_b16_d16_hi v123, v115 offset:1904
	v_lshl_add_u32 v115, v149, 5, s7
	ds_read_b128 v[116:119], v115
	ds_read_b128 v[120:123], v115 offset:16
	s_waitcnt lgkmcnt(1)
	v_add_f32_e32 v115, v116, v117
	v_add_f32_e32 v116, v118, v119
	v_add_f32_e32 v115, v115, v116
	s_waitcnt lgkmcnt(0)
	v_add_f32_e32 v116, v120, v121
	v_add_f32_e32 v115, v115, v116
	v_add_f32_e32 v116, v122, v123
	v_add_f32_e32 v115, v116, v115
	v_fmamk_f32 v115, v115, 0x3b000000, v235
	v_rsq_f32_e32 v115, v115
	s_nop 0
	v_mul_f32_e32 v107, v115, v107
	v_mul_f32_e32 v108, v115, v108
	v_mul_f32_e32 v107, v7, v107
	v_mul_f32_e32 v110, v115, v110
	v_mul_f32_e32 v109, v115, v109
	v_mul_f32_e32 v112, v115, v112
	v_mul_f32_e32 v111, v115, v111
	v_mul_f32_e32 v114, v115, v114
	v_mul_f32_e32 v113, v115, v113
	v_bfe_u32 v115, v0, 8, 2
	v_lshlrev_b32_e32 v115, 3, v115
	v_xor_b32_e32 v115, v115, v149
	v_lshlrev_b32_e32 v115, 1, v115
	v_mul_f32_e32 v110, v8, v110
	v_add3_u32 v115, s20, v115, v0
	v_mul_f32_e32 v109, v9, v109
	v_mul_f32_e32 v112, v2, v112
	v_cvt_pk_bf16_f32 v107, v107, v110
	ds_write_b16 v115, v107 offset:272
	ds_write_b16_d16_hi v115, v107 offset:544
	v_mul_f32_e32 v111, v3, v111
	v_mul_f32_e32 v114, v4, v114
	v_cvt_pk_bf16_f32 v107, v109, v112
	ds_write_b16 v115, v107 offset:816
	ds_write_b16_d16_hi v115, v107 offset:1088
	v_mul_f32_e32 v108, v6, v108
	v_mul_f32_e32 v113, v5, v113
	v_cvt_pk_bf16_f32 v107, v111, v114
	ds_write_b16 v115, v107 offset:1360
	ds_write_b16_d16_hi v115, v107 offset:1632
	v_cvt_pk_bf16_f32 v107, v108, v113
	ds_write_b16 v115, v107
	ds_write_b16_d16_hi v115, v107 offset:1904
	v_lshl_add_u32 v107, v148, 5, s7
	ds_read_b128 v[108:111], v107
	ds_read_b128 v[112:115], v107 offset:16
	s_waitcnt lgkmcnt(1)
	v_add_f32_e32 v107, v108, v109
	v_add_f32_e32 v108, v110, v111
	v_add_f32_e32 v107, v107, v108
	s_waitcnt lgkmcnt(0)
	v_add_f32_e32 v108, v112, v113
	v_add_f32_e32 v107, v107, v108
	v_add_f32_e32 v108, v114, v115
	v_add_f32_e32 v107, v108, v107
	v_fmamk_f32 v107, v107, 0x3b000000, v235
	v_rsq_f32_e32 v107, v107
	s_nop 0
	v_mul_f32_e32 v92, v107, v92
	v_mul_f32_e32 v93, v107, v93
	v_mul_f32_e32 v92, v7, v92
	v_mul_f32_e32 v95, v107, v95
	v_mul_f32_e32 v94, v107, v94
	v_mul_f32_e32 v97, v107, v97
	v_mul_f32_e32 v96, v107, v96
	v_mul_f32_e32 v99, v107, v99
	v_mul_f32_e32 v98, v107, v98
	v_bfe_u32 v107, v0, 8, 2
	v_lshlrev_b32_e32 v107, 3, v107
	v_xor_b32_e32 v107, v107, v148
	v_lshlrev_b32_e32 v107, 1, v107
	v_mul_f32_e32 v95, v8, v95
	v_add3_u32 v107, s20, v107, v0
	v_mul_f32_e32 v94, v9, v94
	v_mul_f32_e32 v97, v2, v97
	v_cvt_pk_bf16_f32 v92, v92, v95
	ds_write_b16 v107, v92 offset:272
	ds_write_b16_d16_hi v107, v92 offset:544
	v_mul_f32_e32 v96, v3, v96
	v_mul_f32_e32 v99, v4, v99
	v_cvt_pk_bf16_f32 v92, v94, v97
	ds_write_b16 v107, v92 offset:816
	ds_write_b16_d16_hi v107, v92 offset:1088
	v_mul_f32_e32 v93, v6, v93
	v_mul_f32_e32 v98, v5, v98
	v_cvt_pk_bf16_f32 v92, v96, v99
	ds_write_b16 v107, v92 offset:1360
	ds_write_b16_d16_hi v107, v92 offset:1632
	v_cvt_pk_bf16_f32 v92, v93, v98
	ds_write_b16 v107, v92
	ds_write_b16_d16_hi v107, v92 offset:1904
	v_lshl_add_u32 v96, v147, 5, s7
	ds_read_b128 v[92:95], v96
	ds_read_b128 v[96:99], v96 offset:16
	s_waitcnt lgkmcnt(1)
	v_add_f32_e32 v92, v92, v93
	v_add_f32_e32 v93, v94, v95
	v_add_f32_e32 v92, v92, v93
	s_waitcnt lgkmcnt(0)
	v_add_f32_e32 v93, v96, v97
	v_add_f32_e32 v92, v92, v93
	v_add_f32_e32 v93, v98, v99
	v_add_f32_e32 v92, v93, v92
	v_fmamk_f32 v92, v92, 0x3b000000, v235
	v_rsq_f32_e32 v92, v92
	s_nop 0
	v_mul_f32_e32 v83, v92, v83
	v_mul_f32_e32 v84, v92, v84
	v_mul_f32_e32 v83, v7, v83
	v_mul_f32_e32 v86, v92, v86
	v_mul_f32_e32 v85, v92, v85
	v_mul_f32_e32 v89, v92, v89
	v_mul_f32_e32 v88, v92, v88
	v_mul_f32_e32 v91, v92, v91
	v_mul_f32_e32 v90, v92, v90
	v_bfe_u32 v92, v0, 8, 2
	v_lshlrev_b32_e32 v92, 3, v92
	v_xor_b32_e32 v92, v92, v147
	v_lshlrev_b32_e32 v92, 1, v92
	v_mul_f32_e32 v86, v8, v86
	v_add3_u32 v92, s20, v92, v0
	v_mul_f32_e32 v85, v9, v85
	v_mul_f32_e32 v89, v2, v89
	v_cvt_pk_bf16_f32 v83, v83, v86
	ds_write_b16 v92, v83 offset:272
	ds_write_b16_d16_hi v92, v83 offset:544
	v_mul_f32_e32 v88, v3, v88
	v_mul_f32_e32 v91, v4, v91
	v_cvt_pk_bf16_f32 v83, v85, v89
	ds_write_b16 v92, v83 offset:816
	ds_write_b16_d16_hi v92, v83 offset:1088
	v_mul_f32_e32 v84, v6, v84
	v_mul_f32_e32 v90, v5, v90
	v_cvt_pk_bf16_f32 v83, v88, v91
	ds_write_b16 v92, v83 offset:1360
	ds_write_b16_d16_hi v92, v83 offset:1632
	v_cvt_pk_bf16_f32 v83, v84, v90
	ds_write_b16 v92, v83
	ds_write_b16_d16_hi v92, v83 offset:1904
	v_lshl_add_u32 v83, v146, 5, s7
	ds_read_b128 v[88:91], v83
	ds_read_b128 v[92:95], v83 offset:16
	s_waitcnt lgkmcnt(1)
	v_add_f32_e32 v83, v88, v89
	v_add_f32_e32 v84, v90, v91
	v_add_f32_e32 v83, v83, v84
	s_waitcnt lgkmcnt(0)
	v_add_f32_e32 v84, v92, v93
	v_add_f32_e32 v83, v83, v84
	v_add_f32_e32 v84, v94, v95
	v_add_f32_e32 v83, v84, v83
	v_fmamk_f32 v83, v83, 0x3b000000, v235
	v_rsq_f32_e32 v83, v83
	s_nop 0
	v_mul_f32_e32 v75, v83, v75
	v_mul_f32_e32 v76, v83, v76
	v_mul_f32_e32 v75, v7, v75
	v_mul_f32_e32 v78, v83, v78
	v_mul_f32_e32 v77, v83, v77
	v_mul_f32_e32 v80, v83, v80
	v_mul_f32_e32 v79, v83, v79
	v_mul_f32_e32 v82, v83, v82
	v_mul_f32_e32 v81, v83, v81
	v_bfe_u32 v83, v0, 8, 2
	v_lshlrev_b32_e32 v83, 3, v83
	v_xor_b32_e32 v83, v83, v146
	v_lshlrev_b32_e32 v83, 1, v83
	v_mul_f32_e32 v78, v8, v78
	v_add3_u32 v83, s20, v83, v0
	v_mul_f32_e32 v77, v9, v77
	v_mul_f32_e32 v80, v2, v80
	v_cvt_pk_bf16_f32 v75, v75, v78
	ds_write_b16 v83, v75 offset:272
	ds_write_b16_d16_hi v83, v75 offset:544
	v_mul_f32_e32 v79, v3, v79
	v_mul_f32_e32 v82, v4, v82
	v_cvt_pk_bf16_f32 v75, v77, v80
	ds_write_b16 v83, v75 offset:816
	ds_write_b16_d16_hi v83, v75 offset:1088
	v_mul_f32_e32 v76, v6, v76
	v_mul_f32_e32 v81, v5, v81
	v_cvt_pk_bf16_f32 v75, v79, v82
	ds_write_b16 v83, v75 offset:1360
	ds_write_b16_d16_hi v83, v75 offset:1632
	v_cvt_pk_bf16_f32 v75, v76, v81
	ds_write_b16 v83, v75
	ds_write_b16_d16_hi v83, v75 offset:1904
	v_lshl_add_u32 v75, v145, 5, s7
	ds_read_b128 v[76:79], v75
	ds_read_b128 v[80:83], v75 offset:16
	s_waitcnt lgkmcnt(1)
	v_add_f32_e32 v75, v76, v77
	v_add_f32_e32 v76, v78, v79
	v_add_f32_e32 v75, v75, v76
	s_waitcnt lgkmcnt(0)
	v_add_f32_e32 v76, v80, v81
	v_add_f32_e32 v75, v75, v76
	v_add_f32_e32 v76, v82, v83
	v_add_f32_e32 v75, v76, v75
	v_fmamk_f32 v75, v75, 0x3b000000, v235
	v_rsq_f32_e32 v75, v75
	s_nop 0
	v_mul_f32_e32 v67, v75, v67
	v_mul_f32_e32 v68, v75, v68
	v_mul_f32_e32 v67, v7, v67
	v_mul_f32_e32 v70, v75, v70
	v_mul_f32_e32 v69, v75, v69
	v_mul_f32_e32 v72, v75, v72
	v_mul_f32_e32 v71, v75, v71
	v_mul_f32_e32 v74, v75, v74
	v_mul_f32_e32 v73, v75, v73
	v_bfe_u32 v75, v0, 8, 2
	v_lshlrev_b32_e32 v75, 3, v75
	v_xor_b32_e32 v75, v75, v145
	v_lshlrev_b32_e32 v75, 1, v75
	v_mul_f32_e32 v70, v8, v70
	v_add3_u32 v75, s20, v75, v0
	v_mul_f32_e32 v69, v9, v69
	v_mul_f32_e32 v72, v2, v72
	v_cvt_pk_bf16_f32 v67, v67, v70
	ds_write_b16 v75, v67 offset:272
	ds_write_b16_d16_hi v75, v67 offset:544
	v_mul_f32_e32 v71, v3, v71
	v_mul_f32_e32 v74, v4, v74
	v_cvt_pk_bf16_f32 v67, v69, v72
	ds_write_b16 v75, v67 offset:816
	ds_write_b16_d16_hi v75, v67 offset:1088
	v_mul_f32_e32 v68, v6, v68
	v_mul_f32_e32 v73, v5, v73
	v_cvt_pk_bf16_f32 v67, v71, v74
	ds_write_b16 v75, v67 offset:1360
	ds_write_b16_d16_hi v75, v67 offset:1632
	v_cvt_pk_bf16_f32 v67, v68, v73
	ds_write_b16 v75, v67
	ds_write_b16_d16_hi v75, v67 offset:1904
	v_lshl_add_u32 v67, v143, 5, s7
	ds_read_b128 v[68:71], v67
	ds_read_b128 v[72:75], v67 offset:16
	s_waitcnt lgkmcnt(1)
	v_add_f32_e32 v67, v68, v69
	v_add_f32_e32 v68, v70, v71
	v_add_f32_e32 v67, v67, v68
	s_waitcnt lgkmcnt(0)
	v_add_f32_e32 v68, v72, v73
	v_add_f32_e32 v67, v67, v68
	v_add_f32_e32 v68, v74, v75
	v_add_f32_e32 v67, v68, v67
	v_fmamk_f32 v67, v67, 0x3b000000, v235
	v_rsq_f32_e32 v67, v67
	s_nop 0
	v_mul_f32_e32 v59, v67, v59
	v_mul_f32_e32 v60, v67, v60
	v_mul_f32_e32 v59, v7, v59
	v_mul_f32_e32 v62, v67, v62
	v_mul_f32_e32 v61, v67, v61
	v_mul_f32_e32 v64, v67, v64
	v_mul_f32_e32 v63, v67, v63
	v_mul_f32_e32 v66, v67, v66
	v_mul_f32_e32 v65, v67, v65
	v_bfe_u32 v67, v0, 8, 2
	v_lshlrev_b32_e32 v67, 3, v67
	v_xor_b32_e32 v67, v67, v143
	v_lshlrev_b32_e32 v67, 1, v67
	v_mul_f32_e32 v62, v8, v62
	v_add3_u32 v67, s20, v67, v0
	v_mul_f32_e32 v61, v9, v61
	v_mul_f32_e32 v64, v2, v64
	v_cvt_pk_bf16_f32 v59, v59, v62
	ds_write_b16 v67, v59 offset:272
	ds_write_b16_d16_hi v67, v59 offset:544
	v_mul_f32_e32 v63, v3, v63
	v_mul_f32_e32 v66, v4, v66
	v_cvt_pk_bf16_f32 v59, v61, v64
	ds_write_b16 v67, v59 offset:816
	ds_write_b16_d16_hi v67, v59 offset:1088
	v_mul_f32_e32 v60, v6, v60
	v_mul_f32_e32 v65, v5, v65
	v_cvt_pk_bf16_f32 v59, v63, v66
	ds_write_b16 v67, v59 offset:1360
	ds_write_b16_d16_hi v67, v59 offset:1632
	v_cvt_pk_bf16_f32 v59, v60, v65
	ds_write_b16 v67, v59
	ds_write_b16_d16_hi v67, v59 offset:1904
	v_lshl_add_u32 v59, v134, 5, s7
	ds_read_b128 v[60:63], v59
	ds_read_b128 v[64:67], v59 offset:16
	s_waitcnt lgkmcnt(1)
	v_add_f32_e32 v59, v60, v61
	v_add_f32_e32 v60, v62, v63
	v_add_f32_e32 v59, v59, v60
	s_waitcnt lgkmcnt(0)
	v_add_f32_e32 v60, v64, v65
	v_add_f32_e32 v59, v59, v60
	v_add_f32_e32 v60, v66, v67
	v_add_f32_e32 v59, v60, v59
	v_fmamk_f32 v59, v59, 0x3b000000, v235
	v_rsq_f32_e32 v59, v59
	s_nop 0
	v_mul_f32_e32 v51, v59, v51
	v_mul_f32_e32 v52, v59, v52
	v_mul_f32_e32 v51, v7, v51
	v_mul_f32_e32 v54, v59, v54
	v_mul_f32_e32 v53, v59, v53
	v_mul_f32_e32 v56, v59, v56
	v_mul_f32_e32 v55, v59, v55
	v_mul_f32_e32 v58, v59, v58
	v_mul_f32_e32 v57, v59, v57
	v_bfe_u32 v59, v0, 8, 2
	v_lshlrev_b32_e32 v59, 3, v59
	v_xor_b32_e32 v59, v59, v134
	v_lshlrev_b32_e32 v59, 1, v59
	v_mul_f32_e32 v54, v8, v54
	v_add3_u32 v59, s20, v59, v0
	v_mul_f32_e32 v53, v9, v53
	v_mul_f32_e32 v56, v2, v56
	v_cvt_pk_bf16_f32 v51, v51, v54
	ds_write_b16 v59, v51 offset:272
	ds_write_b16_d16_hi v59, v51 offset:544
	v_mul_f32_e32 v55, v3, v55
	v_mul_f32_e32 v58, v4, v58
	v_cvt_pk_bf16_f32 v51, v53, v56
	ds_write_b16 v59, v51 offset:816
	ds_write_b16_d16_hi v59, v51 offset:1088
	v_mul_f32_e32 v52, v6, v52
	v_mul_f32_e32 v57, v5, v57
	v_cvt_pk_bf16_f32 v51, v55, v58
	ds_write_b16 v59, v51 offset:1360
	ds_write_b16_d16_hi v59, v51 offset:1632
	v_cvt_pk_bf16_f32 v51, v52, v57
	ds_write_b16 v59, v51
	ds_write_b16_d16_hi v59, v51 offset:1904
	v_lshl_add_u32 v51, v133, 5, s7
	ds_read_b128 v[52:55], v51
	ds_read_b128 v[56:59], v51 offset:16
	s_waitcnt lgkmcnt(1)
	v_add_f32_e32 v51, v52, v53
	v_add_f32_e32 v52, v54, v55
	v_add_f32_e32 v51, v51, v52
	s_waitcnt lgkmcnt(0)
	v_add_f32_e32 v52, v56, v57
	v_add_f32_e32 v51, v51, v52
	v_add_f32_e32 v52, v58, v59
	v_add_f32_e32 v51, v52, v51
	v_fmamk_f32 v51, v51, 0x3b000000, v235
	v_rsq_f32_e32 v51, v51
	s_nop 0
	v_mul_f32_e32 v42, v51, v42
	v_mul_f32_e32 v43, v51, v43
	v_mul_f32_e32 v42, v7, v42
	v_mul_f32_e32 v45, v51, v45
	v_mul_f32_e32 v44, v51, v44
	v_mul_f32_e32 v47, v51, v47
	v_mul_f32_e32 v46, v51, v46
	v_mul_f32_e32 v50, v51, v50
	v_mul_f32_e32 v48, v51, v48
	v_bfe_u32 v51, v0, 8, 2
	v_lshlrev_b32_e32 v51, 3, v51
	v_xor_b32_e32 v51, v51, v133
	v_lshlrev_b32_e32 v51, 1, v51
	v_mul_f32_e32 v45, v8, v45
	v_add3_u32 v51, s20, v51, v0
	v_mul_f32_e32 v44, v9, v44
	v_mul_f32_e32 v47, v2, v47
	v_cvt_pk_bf16_f32 v42, v42, v45
	ds_write_b16 v51, v42 offset:272
	ds_write_b16_d16_hi v51, v42 offset:544
	v_mul_f32_e32 v46, v3, v46
	v_mul_f32_e32 v50, v4, v50
	v_cvt_pk_bf16_f32 v42, v44, v47
	ds_write_b16 v51, v42 offset:816
	ds_write_b16_d16_hi v51, v42 offset:1088
	v_mul_f32_e32 v43, v6, v43
	v_mul_f32_e32 v48, v5, v48
	v_cvt_pk_bf16_f32 v42, v46, v50
	ds_write_b16 v51, v42 offset:1360
	ds_write_b16_d16_hi v51, v42 offset:1632
	v_cvt_pk_bf16_f32 v42, v43, v48
	ds_write_b16 v51, v42
	ds_write_b16_d16_hi v51, v42 offset:1904
	v_lshl_add_u32 v46, v132, 5, s7
	ds_read_b128 v[42:45], v46
	ds_read_b128 v[50:53], v46 offset:16
	s_waitcnt lgkmcnt(1)
	v_add_f32_e32 v42, v42, v43
	v_add_f32_e32 v43, v44, v45
	v_add_f32_e32 v42, v42, v43
	s_waitcnt lgkmcnt(0)
	v_add_f32_e32 v43, v50, v51
	v_add_f32_e32 v42, v42, v43
	v_add_f32_e32 v43, v52, v53
	v_add_f32_e32 v42, v43, v42
	v_fmamk_f32 v42, v42, 0x3b000000, v235
	v_rsq_f32_e32 v42, v42
	s_nop 0
	v_mul_f32_e32 v34, v42, v34
	v_mul_f32_e32 v35, v42, v35
	v_mul_f32_e32 v34, v7, v34
	v_mul_f32_e32 v37, v42, v37
	v_mul_f32_e32 v36, v42, v36
	v_mul_f32_e32 v39, v42, v39
	v_mul_f32_e32 v38, v42, v38
	v_mul_f32_e32 v41, v42, v41
	v_mul_f32_e32 v40, v42, v40
	v_bfe_u32 v42, v0, 8, 2
	v_lshlrev_b32_e32 v42, 3, v42
	v_xor_b32_e32 v42, v42, v132
	v_lshlrev_b32_e32 v42, 1, v42
	v_mul_f32_e32 v37, v8, v37
	v_add3_u32 v42, s20, v42, v0
	v_mul_f32_e32 v36, v9, v36
	v_mul_f32_e32 v39, v2, v39
	v_cvt_pk_bf16_f32 v34, v34, v37
	ds_write_b16 v42, v34 offset:272
	ds_write_b16_d16_hi v42, v34 offset:544
	v_mul_f32_e32 v38, v3, v38
	v_mul_f32_e32 v41, v4, v41
	v_cvt_pk_bf16_f32 v34, v36, v39
	ds_write_b16 v42, v34 offset:816
	ds_write_b16_d16_hi v42, v34 offset:1088
	v_mul_f32_e32 v35, v6, v35
	v_mul_f32_e32 v40, v5, v40
	v_cvt_pk_bf16_f32 v34, v38, v41
	ds_write_b16 v42, v34 offset:1360
	ds_write_b16_d16_hi v42, v34 offset:1632
	v_cvt_pk_bf16_f32 v34, v35, v40
	ds_write_b16 v42, v34
	ds_write_b16_d16_hi v42, v34 offset:1904
	v_lshl_add_u32 v38, v128, 5, s7
	ds_read_b128 v[34:37], v38
	ds_read_b128 v[38:41], v38 offset:16
	s_waitcnt lgkmcnt(1)
	v_add_f32_e32 v34, v34, v35
	v_add_f32_e32 v35, v36, v37
	v_add_f32_e32 v34, v34, v35
	s_waitcnt lgkmcnt(0)
	v_add_f32_e32 v35, v38, v39
	v_add_f32_e32 v34, v34, v35
	v_add_f32_e32 v35, v40, v41
	v_add_f32_e32 v34, v35, v34
	v_fmamk_f32 v34, v34, 0x3b000000, v235
	v_rsq_f32_e32 v34, v34
	s_nop 0
	v_mul_f32_e32 v26, v34, v26
	v_mul_f32_e32 v27, v34, v27
	v_mul_f32_e32 v26, v7, v26
	v_mul_f32_e32 v29, v34, v29
	v_mul_f32_e32 v28, v34, v28
	v_mul_f32_e32 v31, v34, v31
	v_mul_f32_e32 v30, v34, v30
	v_mul_f32_e32 v33, v34, v33
	v_mul_f32_e32 v32, v34, v32
	v_bfe_u32 v34, v0, 8, 2
	v_lshlrev_b32_e32 v34, 3, v34
	v_xor_b32_e32 v34, v34, v128
	v_lshlrev_b32_e32 v34, 1, v34
	v_mul_f32_e32 v29, v8, v29
	v_add3_u32 v34, s20, v34, v0
	v_mul_f32_e32 v28, v9, v28
	v_mul_f32_e32 v31, v2, v31
	v_cvt_pk_bf16_f32 v26, v26, v29
	ds_write_b16 v34, v26 offset:272
	ds_write_b16_d16_hi v34, v26 offset:544
	v_mul_f32_e32 v30, v3, v30
	v_mul_f32_e32 v33, v4, v33
	v_cvt_pk_bf16_f32 v26, v28, v31
	ds_write_b16 v34, v26 offset:816
	ds_write_b16_d16_hi v34, v26 offset:1088
	v_mul_f32_e32 v27, v6, v27
	v_mul_f32_e32 v32, v5, v32
	v_cvt_pk_bf16_f32 v26, v30, v33
	ds_write_b16 v34, v26 offset:1360
	ds_write_b16_d16_hi v34, v26 offset:1632
	v_cvt_pk_bf16_f32 v26, v27, v32
	ds_write_b16 v34, v26
	ds_write_b16_d16_hi v34, v26 offset:1904
	v_lshl_add_u32 v30, v87, 5, s7
	ds_read_b128 v[26:29], v30
	ds_read_b128 v[30:33], v30 offset:16
	s_waitcnt lgkmcnt(1)
	v_add_f32_e32 v26, v26, v27
	v_add_f32_e32 v27, v28, v29
	v_add_f32_e32 v26, v26, v27
	s_waitcnt lgkmcnt(0)
	v_add_f32_e32 v27, v30, v31
	v_add_f32_e32 v26, v26, v27
	v_add_f32_e32 v27, v32, v33
	v_add_f32_e32 v26, v27, v26
	v_fmamk_f32 v26, v26, 0x3b000000, v235
	v_rsq_f32_e32 v26, v26
	s_nop 0
	v_mul_f32_e32 v18, v26, v18
	v_mul_f32_e32 v19, v26, v19
	v_mul_f32_e32 v18, v7, v18
	v_mul_f32_e32 v21, v26, v21
	v_mul_f32_e32 v20, v26, v20
	v_mul_f32_e32 v23, v26, v23
	v_mul_f32_e32 v22, v26, v22
	v_mul_f32_e32 v25, v26, v25
	v_mul_f32_e32 v24, v26, v24
	v_bfe_u32 v26, v0, 8, 2
	v_lshlrev_b32_e32 v26, 3, v26
	v_xor_b32_e32 v26, v26, v87
	v_lshlrev_b32_e32 v26, 1, v26
	v_mul_f32_e32 v21, v8, v21
	v_add3_u32 v26, s20, v26, v0
	v_mul_f32_e32 v20, v9, v20
	v_mul_f32_e32 v23, v2, v23
	v_cvt_pk_bf16_f32 v18, v18, v21
	ds_write_b16 v26, v18 offset:272
	ds_write_b16_d16_hi v26, v18 offset:544
	v_mul_f32_e32 v22, v3, v22
	v_mul_f32_e32 v25, v4, v25
	v_cvt_pk_bf16_f32 v18, v20, v23
	ds_write_b16 v26, v18 offset:816
	ds_write_b16_d16_hi v26, v18 offset:1088
	v_mul_f32_e32 v19, v6, v19
	v_mul_f32_e32 v24, v5, v24
	v_cvt_pk_bf16_f32 v18, v22, v25
	ds_write_b16 v26, v18 offset:1360
	ds_write_b16_d16_hi v26, v18 offset:1632
	v_cvt_pk_bf16_f32 v18, v19, v24
	ds_write_b16 v26, v18
	ds_write_b16_d16_hi v26, v18 offset:1904
	v_lshl_add_u32 v22, v49, 5, s7
	ds_read_b128 v[18:21], v22
	ds_read_b128 v[22:25], v22 offset:16
	s_waitcnt lgkmcnt(1)
	v_add_f32_e32 v18, v18, v19
	v_add_f32_e32 v19, v20, v21
	v_add_f32_e32 v18, v18, v19
	s_waitcnt lgkmcnt(0)
	v_add_f32_e32 v19, v22, v23
	v_add_f32_e32 v18, v18, v19
	v_add_f32_e32 v19, v24, v25
	v_add_f32_e32 v18, v19, v18
	v_fmamk_f32 v18, v18, 0x3b000000, v235
	v_rsq_f32_e32 v18, v18
	s_nop 0
	v_mul_f32_e32 v10, v18, v10
	v_mul_f32_e32 v7, v7, v10
	v_mul_f32_e32 v10, v18, v13
	v_mul_f32_e32 v8, v8, v10
	v_mul_f32_e32 v10, v18, v12
	v_mul_f32_e32 v9, v9, v10
	v_mul_f32_e32 v10, v18, v15
	v_mul_f32_e32 v2, v2, v10
	v_mul_f32_e32 v10, v18, v14
	v_mul_f32_e32 v3, v3, v10
	v_mul_f32_e32 v10, v18, v17
	v_mul_f32_e32 v11, v18, v11
	v_mul_f32_e32 v4, v4, v10
	v_mul_f32_e32 v10, v18, v16
	v_mul_f32_e32 v6, v6, v11
	v_mul_f32_e32 v5, v5, v10
	v_bfe_u32 v10, v0, 8, 2
	v_lshlrev_b32_e32 v10, 3, v10
	v_xor_b32_e32 v10, v10, v49
	v_lshlrev_b32_e32 v10, 1, v10
	v_add3_u32 v0, s20, v10, v0
	v_cvt_pk_bf16_f32 v2, v6, v2
	ds_write_b16 v0, v2
	ds_write_b16_d16_hi v0, v2 offset:1088
	v_cvt_pk_bf16_f32 v2, v7, v3
	ds_write_b16 v0, v2 offset:272
	ds_write_b16_d16_hi v0, v2 offset:1360
	v_cvt_pk_bf16_f32 v2, v8, v4
	ds_write_b16 v0, v2 offset:544
	ds_write_b16_d16_hi v0, v2 offset:1632
	v_cvt_pk_bf16_f32 v2, v9, v5
	ds_write_b16 v0, v2 offset:816
	ds_write_b16_d16_hi v0, v2 offset:1904
	v_lshlrev_b32_e32 v0, 4, v106
	v_lshlrev_b32_e32 v4, 2, v106
	v_lshl_add_u64 v[2:3], s[4:5], 0, v[0:1]
	v_lshl_or_b32 v54, s12, 7, v4
	v_lshlrev_b32_e32 v4, 8, v105
	v_mov_b32_e32 v5, v1
	v_lshl_add_u64 v[82:83], v[2:3], 0, v[4:5]
	s_mov_b64 s[4:5], 0x1620000
	v_lshl_add_u64 v[6:7], v[82:83], 0, s[4:5]
	s_mov_b32 s4, 0x1620000
	v_add_co_u32_e32 v2, vcc, s4, v82
	s_waitcnt lgkmcnt(0)
	s_nop 0
	v_addc_co_u32_e32 v3, vcc, 0, v83, vcc
	s_barrier
	global_load_dwordx4 v[2:5], v[2:3], off
	s_nop 0
	global_load_dwordx4 v[50:53], v[6:7], off offset:32
	v_mul_u32_u24_e32 v8, 0x110, v105
	v_and_b32_e32 v42, 16, v105
	v_xor_b32_e32 v0, v42, v0
	v_add3_u32 v0, s20, v8, v0
	ds_read_b128 v[42:45], v0 offset:8736
	ds_read_b128 v[46:49], v0
	ds_read_b128 v[38:41], v0 offset:32
	s_waitcnt vmcnt(1) lgkmcnt(1)
	v_mfma_f32_32x32x16_bf16 v[18:33], v[2:5], v[46:49], 0
	ds_read_b128 v[34:37], v0 offset:8704
	v_ashrrev_i32_e32 v55, 31, v54
	v_lshl_add_u64 v[98:99], v[54:55], 2, s[16:17]
	s_mov_b32 s4, 0x1622000
	v_mfma_f32_32x32x16_bf16 v[2:17], v[2:5], v[42:45], 0
	s_waitcnt vmcnt(0) lgkmcnt(1)
	v_mfma_f32_32x32x16_bf16 v[18:33], v[50:53], v[38:41], v[18:33]
	s_waitcnt lgkmcnt(0)
	v_mfma_f32_32x32x16_bf16 v[2:17], v[50:53], v[34:37], v[2:17]
	global_load_dwordx4 v[50:53], v[98:99], off
	global_load_dwordx4 v[54:57], v[98:99], off offset:32
	global_load_dwordx4 v[58:61], v[98:99], off offset:64
	global_load_dwordx4 v[62:65], v[98:99], off offset:96
	s_nop 5
	v_mov_b32_e32 v66, v18
	s_nop 0
	v_mov_b32_e32 v67, v2
	v_mov_b32_e32 v2, v19
	s_waitcnt vmcnt(3)
	v_pk_add_f32 v[2:3], v[2:3], v[50:51] op_sel:[0,1]
	s_nop 0
	v_cvt_pk_bf16_f32 v108, v2, v3
	v_mov_b32_e32 v2, v20
	v_mov_b32_e32 v3, v4
	v_pk_add_f32 v[2:3], v[2:3], v[52:53] op_sel_hi:[1,0]
	v_mov_b32_e32 v4, v21
	v_cvt_pk_bf16_f32 v109, v2, v3
	v_mov_b32_e32 v2, v53
	v_pk_add_f32 v[2:3], v[4:5], v[2:3] op_sel_hi:[1,0]
	v_pk_add_f32 v[66:67], v[66:67], v[50:51] op_sel_hi:[1,0]
	v_cvt_pk_bf16_f32 v110, v2, v3
	v_mov_b32_e32 v2, v22
	v_mov_b32_e32 v3, v6
	s_waitcnt vmcnt(2)
	v_pk_add_f32 v[2:3], v[2:3], v[54:55] op_sel_hi:[1,0]
	v_mov_b32_e32 v6, v23
	v_cvt_pk_bf16_f32 v111, v2, v3
	v_pk_add_f32 v[2:3], v[6:7], v[54:55] op_sel:[0,1]
	v_add_co_u32_e32 v6, vcc, s4, v82
	v_cvt_pk_bf16_f32 v112, v2, v3
	v_mov_b32_e32 v2, v24
	v_mov_b32_e32 v3, v8
	v_pk_add_f32 v[2:3], v[2:3], v[56:57] op_sel_hi:[1,0]
	v_mov_b32_e32 v8, v25
	v_cvt_pk_bf16_f32 v113, v2, v3
	v_mov_b32_e32 v2, v57
	v_pk_add_f32 v[2:3], v[8:9], v[2:3] op_sel_hi:[1,0]
	v_addc_co_u32_e32 v7, vcc, 0, v83, vcc
	v_cvt_pk_bf16_f32 v114, v2, v3
	v_mov_b32_e32 v2, v26
	v_mov_b32_e32 v3, v10
	s_waitcnt vmcnt(1)
	v_pk_add_f32 v[2:3], v[2:3], v[58:59] op_sel_hi:[1,0]
	v_mov_b32_e32 v10, v27
	v_cvt_pk_bf16_f32 v115, v2, v3
	v_pk_add_f32 v[2:3], v[10:11], v[58:59] op_sel:[0,1]
	v_cvt_pk_bf16_f32 v107, v66, v67
	v_cvt_pk_bf16_f32 v116, v2, v3
	v_mov_b32_e32 v2, v28
	v_mov_b32_e32 v3, v12
	v_pk_add_f32 v[2:3], v[2:3], v[60:61] op_sel_hi:[1,0]
	v_mov_b32_e32 v12, v29
	v_cvt_pk_bf16_f32 v117, v2, v3
	v_mov_b32_e32 v2, v61
	v_pk_add_f32 v[2:3], v[12:13], v[2:3] op_sel_hi:[1,0]
	s_mov_b32 s4, 0x1624000
	v_cvt_pk_bf16_f32 v118, v2, v3
	v_mov_b32_e32 v2, v30
	v_mov_b32_e32 v3, v14
	s_waitcnt vmcnt(0)
	v_pk_add_f32 v[2:3], v[2:3], v[62:63] op_sel_hi:[1,0]
	v_mov_b32_e32 v14, v31
	v_cvt_pk_bf16_f32 v119, v2, v3
	v_pk_add_f32 v[2:3], v[14:15], v[62:63] op_sel:[0,1]
	s_nop 0
	v_cvt_pk_bf16_f32 v120, v2, v3
	v_mov_b32_e32 v2, v32
	v_mov_b32_e32 v3, v16
	v_pk_add_f32 v[2:3], v[2:3], v[64:65] op_sel_hi:[1,0]
	v_mov_b32_e32 v16, v33
	v_cvt_pk_bf16_f32 v121, v2, v3
	v_mov_b32_e32 v2, v65
	v_pk_add_f32 v[2:3], v[16:17], v[2:3] op_sel_hi:[1,0]
	s_nop 0
	v_cvt_pk_bf16_f32 v122, v2, v3
	global_load_dwordx4 v[2:5], v[6:7], off
	global_load_dwordx4 v[50:53], v[6:7], off offset:32
	global_load_dwordx4 v[54:57], v[6:7], off offset:64
	global_load_dwordx4 v[66:69], v[6:7], off offset:96
	s_waitcnt vmcnt(3)
	v_mfma_f32_32x32x16_bf16 v[18:33], v[2:5], v[46:49], 0
	ds_read_b128 v[62:65], v0 offset:64
	ds_read_b128 v[58:61], v0 offset:8800
	v_mfma_f32_32x32x16_bf16 v[2:17], v[2:5], v[42:45], 0
	s_waitcnt vmcnt(2)
	v_mfma_f32_32x32x16_bf16 v[18:33], v[50:53], v[38:41], v[18:33]
	v_mfma_f32_32x32x16_bf16 v[2:17], v[50:53], v[34:37], v[2:17]
	s_waitcnt vmcnt(1) lgkmcnt(1)
	v_mfma_f32_32x32x16_bf16 v[18:33], v[54:57], v[62:65], v[18:33]
	s_waitcnt lgkmcnt(0)
	v_mfma_f32_32x32x16_bf16 v[2:17], v[54:57], v[58:61], v[2:17]
	ds_read_b128 v[50:53], v0 offset:96
	ds_read_b128 v[54:57], v0 offset:8768
	s_waitcnt vmcnt(0) lgkmcnt(1)
	v_mfma_f32_32x32x16_bf16 v[18:33], v[66:69], v[50:53], v[18:33]
	s_waitcnt lgkmcnt(0)
	v_mfma_f32_32x32x16_bf16 v[2:17], v[66:69], v[54:57], v[2:17]
	global_load_dwordx4 v[66:69], v[98:99], off offset:128
	global_load_dwordx4 v[70:73], v[98:99], off offset:160
	global_load_dwordx4 v[74:77], v[98:99], off offset:192
	global_load_dwordx4 v[78:81], v[98:99], off offset:224
	s_nop 5
	v_mov_b32_e32 v84, v18
	s_nop 0
	v_mov_b32_e32 v85, v2
	v_mov_b32_e32 v2, v19
	s_waitcnt vmcnt(3)
	v_pk_add_f32 v[2:3], v[2:3], v[66:67] op_sel:[0,1]
	s_nop 0
	v_cvt_pk_bf16_f32 v124, v2, v3
	v_mov_b32_e32 v2, v20
	v_mov_b32_e32 v3, v4
	v_pk_add_f32 v[2:3], v[2:3], v[68:69] op_sel_hi:[1,0]
	v_mov_b32_e32 v4, v21
	v_cvt_pk_bf16_f32 v125, v2, v3
	v_mov_b32_e32 v2, v69
	v_pk_add_f32 v[2:3], v[4:5], v[2:3] op_sel_hi:[1,0]
	v_pk_add_f32 v[84:85], v[84:85], v[66:67] op_sel_hi:[1,0]
	v_cvt_pk_bf16_f32 v126, v2, v3
	v_mov_b32_e32 v2, v22
	v_mov_b32_e32 v3, v6
	s_waitcnt vmcnt(2)
	v_pk_add_f32 v[2:3], v[2:3], v[70:71] op_sel_hi:[1,0]
	v_mov_b32_e32 v6, v23
	v_cvt_pk_bf16_f32 v127, v2, v3
	v_pk_add_f32 v[2:3], v[6:7], v[70:71] op_sel:[0,1]
	v_cvt_pk_bf16_f32 v123, v84, v85
	v_cvt_pk_bf16_f32 v128, v2, v3
	v_mov_b32_e32 v2, v24
	v_mov_b32_e32 v3, v8
	v_pk_add_f32 v[2:3], v[2:3], v[72:73] op_sel_hi:[1,0]
	v_mov_b32_e32 v8, v25
	v_cvt_pk_bf16_f32 v129, v2, v3
	v_mov_b32_e32 v2, v73
	v_pk_add_f32 v[2:3], v[8:9], v[2:3] op_sel_hi:[1,0]
	s_nop 0
	v_cvt_pk_bf16_f32 v130, v2, v3
	v_mov_b32_e32 v2, v26
	v_mov_b32_e32 v3, v10
	s_waitcnt vmcnt(1)
	v_pk_add_f32 v[2:3], v[2:3], v[74:75] op_sel_hi:[1,0]
	v_mov_b32_e32 v10, v27
	v_cvt_pk_bf16_f32 v131, v2, v3
	v_pk_add_f32 v[2:3], v[10:11], v[74:75] op_sel:[0,1]
	s_nop 0
	v_cvt_pk_bf16_f32 v132, v2, v3
	v_mov_b32_e32 v2, v28
	v_mov_b32_e32 v3, v12
	v_pk_add_f32 v[2:3], v[2:3], v[76:77] op_sel_hi:[1,0]
	v_mov_b32_e32 v12, v29
	v_cvt_pk_bf16_f32 v133, v2, v3
	v_mov_b32_e32 v2, v77
	v_pk_add_f32 v[2:3], v[12:13], v[2:3] op_sel_hi:[1,0]
	s_nop 0
	v_cvt_pk_bf16_f32 v134, v2, v3
	v_mov_b32_e32 v2, v30
	v_mov_b32_e32 v3, v14
	s_waitcnt vmcnt(0)
	v_pk_add_f32 v[2:3], v[2:3], v[78:79] op_sel_hi:[1,0]
	v_mov_b32_e32 v14, v31
	v_cvt_pk_bf16_f32 v135, v2, v3
	v_pk_add_f32 v[2:3], v[14:15], v[78:79] op_sel:[0,1]
	s_nop 0
	v_cvt_pk_bf16_f32 v136, v2, v3
	v_mov_b32_e32 v2, v32
	v_mov_b32_e32 v3, v16
	v_pk_add_f32 v[2:3], v[2:3], v[80:81] op_sel_hi:[1,0]
	v_mov_b32_e32 v16, v33
	v_cvt_pk_bf16_f32 v137, v2, v3
	v_mov_b32_e32 v2, v81
	v_pk_add_f32 v[2:3], v[16:17], v[2:3] op_sel_hi:[1,0]
	s_nop 0
	v_cvt_pk_bf16_f32 v138, v2, v3
	v_add_co_u32_e32 v2, vcc, s4, v82
	s_mov_b32 s4, 0x1626000
	s_nop 0
	v_addc_co_u32_e32 v3, vcc, 0, v83, vcc
	global_load_dwordx4 v[18:21], v[2:3], off
	global_load_dwordx4 v[66:69], v[2:3], off offset:32
	global_load_dwordx4 v[70:73], v[2:3], off offset:64
	global_load_dwordx4 v[74:77], v[2:3], off offset:96
	global_load_dwordx4 v[78:81], v[2:3], off offset:128
	global_load_dwordx4 v[84:87], v[2:3], off offset:160
	s_waitcnt vmcnt(5)
	v_mfma_f32_32x32x16_bf16 v[2:17], v[18:21], v[46:49], 0
	v_mfma_f32_32x32x16_bf16 v[18:33], v[18:21], v[42:45], 0
	s_waitcnt vmcnt(4)
	v_mfma_f32_32x32x16_bf16 v[2:17], v[66:69], v[38:41], v[2:17]
	v_mfma_f32_32x32x16_bf16 v[18:33], v[66:69], v[34:37], v[18:33]
	s_waitcnt vmcnt(3)
	v_mfma_f32_32x32x16_bf16 v[2:17], v[70:73], v[62:65], v[2:17]
	v_mfma_f32_32x32x16_bf16 v[18:33], v[70:73], v[58:61], v[18:33]
	ds_read_b128 v[66:69], v0 offset:128
	ds_read_b128 v[70:73], v0 offset:8864
	s_waitcnt vmcnt(2)
	v_mfma_f32_32x32x16_bf16 v[2:17], v[74:77], v[50:53], v[2:17]
	v_mfma_f32_32x32x16_bf16 v[18:33], v[74:77], v[54:57], v[18:33]
	s_waitcnt vmcnt(1) lgkmcnt(1)
	v_mfma_f32_32x32x16_bf16 v[2:17], v[78:81], v[66:69], v[2:17]
	s_waitcnt lgkmcnt(0)
	v_mfma_f32_32x32x16_bf16 v[18:33], v[78:81], v[70:73], v[18:33]
	ds_read_b128 v[74:77], v0 offset:160
	ds_read_b128 v[78:81], v0 offset:8832
	s_waitcnt vmcnt(0) lgkmcnt(1)
	v_mfma_f32_32x32x16_bf16 v[2:17], v[84:87], v[74:77], v[2:17]
	s_waitcnt lgkmcnt(0)
	v_mfma_f32_32x32x16_bf16 v[18:33], v[84:87], v[78:81], v[18:33]
	global_load_dwordx4 v[84:87], v[98:99], off offset:256
	global_load_dwordx4 v[88:91], v[98:99], off offset:288
	global_load_dwordx4 v[92:95], v[98:99], off offset:320
	global_load_dwordx4 v[156:159], v[98:99], off offset:352
	s_nop 5
	v_mov_b32_e32 v96, v2
	s_nop 0
	v_mov_b32_e32 v97, v18
	v_mov_b32_e32 v18, v3
	s_waitcnt vmcnt(3)
	v_pk_add_f32 v[2:3], v[18:19], v[84:85] op_sel:[0,1]
	s_nop 0
	v_cvt_pk_bf16_f32 v150, v2, v3
	v_mov_b32_e32 v2, v4
	v_mov_b32_e32 v3, v20
	v_pk_add_f32 v[2:3], v[2:3], v[86:87] op_sel_hi:[1,0]
	v_mov_b32_e32 v20, v5
	v_cvt_pk_bf16_f32 v151, v2, v3
	v_mov_b32_e32 v2, v87
	v_pk_add_f32 v[2:3], v[20:21], v[2:3] op_sel_hi:[1,0]
	v_pk_add_f32 v[96:97], v[96:97], v[84:85] op_sel_hi:[1,0]
	v_cvt_pk_bf16_f32 v152, v2, v3
	v_mov_b32_e32 v2, v6
	v_mov_b32_e32 v3, v22
	s_waitcnt vmcnt(2)
	v_pk_add_f32 v[2:3], v[2:3], v[88:89] op_sel_hi:[1,0]
	v_mov_b32_e32 v22, v7
	v_cvt_pk_bf16_f32 v153, v2, v3
	v_pk_add_f32 v[2:3], v[22:23], v[88:89] op_sel:[0,1]
	v_cvt_pk_bf16_f32 v154, v96, v97
	v_cvt_pk_bf16_f32 v146, v2, v3
	v_mov_b32_e32 v2, v8
	v_mov_b32_e32 v3, v24
	v_pk_add_f32 v[2:3], v[2:3], v[90:91] op_sel_hi:[1,0]
	v_mov_b32_e32 v24, v9
	v_cvt_pk_bf16_f32 v147, v2, v3
	v_mov_b32_e32 v2, v91
	v_pk_add_f32 v[2:3], v[24:25], v[2:3] op_sel_hi:[1,0]
	s_nop 0
	v_cvt_pk_bf16_f32 v148, v2, v3
	v_mov_b32_e32 v2, v10
	v_mov_b32_e32 v3, v26
	s_waitcnt vmcnt(1)
	v_pk_add_f32 v[2:3], v[2:3], v[92:93] op_sel_hi:[1,0]
	v_mov_b32_e32 v26, v11
	v_cvt_pk_bf16_f32 v149, v2, v3
	v_pk_add_f32 v[2:3], v[26:27], v[92:93] op_sel:[0,1]
	s_nop 0
	v_cvt_pk_bf16_f32 v142, v2, v3
	v_mov_b32_e32 v2, v12
	v_mov_b32_e32 v3, v28
	v_pk_add_f32 v[2:3], v[2:3], v[94:95] op_sel_hi:[1,0]
	v_mov_b32_e32 v28, v13
	v_cvt_pk_bf16_f32 v143, v2, v3
	v_mov_b32_e32 v2, v95
	v_pk_add_f32 v[2:3], v[28:29], v[2:3] op_sel_hi:[1,0]
	s_nop 0
	v_cvt_pk_bf16_f32 v144, v2, v3
	v_mov_b32_e32 v2, v14
	v_mov_b32_e32 v3, v30
	s_waitcnt vmcnt(0)
	v_pk_add_f32 v[2:3], v[2:3], v[156:157] op_sel_hi:[1,0]
	v_mov_b32_e32 v30, v15
	v_cvt_pk_bf16_f32 v145, v2, v3
	v_pk_add_f32 v[2:3], v[30:31], v[156:157] op_sel:[0,1]
	s_nop 0
	v_cvt_pk_bf16_f32 v139, v2, v3
	v_mov_b32_e32 v2, v16
	v_mov_b32_e32 v3, v32
	v_pk_add_f32 v[2:3], v[2:3], v[158:159] op_sel_hi:[1,0]
	v_mov_b32_e32 v32, v17
	v_cvt_pk_bf16_f32 v140, v2, v3
	v_mov_b32_e32 v2, v159
	v_pk_add_f32 v[2:3], v[32:33], v[2:3] op_sel_hi:[1,0]
	s_nop 0
	v_cvt_pk_bf16_f32 v141, v2, v3
	v_add_co_u32_e32 v2, vcc, s4, v82
	s_ashr_i32 s4, s23, 31
	s_nop 0
	v_addc_co_u32_e32 v3, vcc, 0, v83, vcc
	global_load_dwordx4 v[18:21], v[2:3], off
	global_load_dwordx4 v[82:85], v[2:3], off offset:32
	global_load_dwordx4 v[86:89], v[2:3], off offset:64
	global_load_dwordx4 v[90:93], v[2:3], off offset:96
	global_load_dwordx4 v[94:97], v[2:3], off offset:128
	global_load_dwordx4 v[156:159], v[2:3], off offset:160
	global_load_dwordx4 v[160:163], v[2:3], off offset:192
	global_load_dwordx4 v[164:167], v[2:3], off offset:224
	s_waitcnt vmcnt(7)
	v_mfma_f32_32x32x16_bf16 v[2:17], v[18:21], v[46:49], 0
	s_add_u32 s20, s8, s23
	s_addc_u32 s21, s9, s4
	s_add_u32 s16, s20, 0xffffff88
	s_addc_u32 s17, s21, -1
	s_lshl_b64 s[4:5], s[16:17], 11
	v_mfma_f32_32x32x16_bf16 v[18:33], v[18:21], v[42:45], 0
	s_waitcnt vmcnt(6)
	v_mfma_f32_32x32x16_bf16 v[2:17], v[82:85], v[38:41], v[2:17]
	v_mfma_f32_32x32x16_bf16 v[18:33], v[82:85], v[34:37], v[18:33]
	ds_read_b128 v[34:37], v0 offset:192
	ds_read_b128 v[38:41], v0 offset:8928
	v_or_b32_e32 v82, s6, v105
	v_lshlrev_b32_e32 v82, 1, v82
	v_mul_u32_u24_e32 v83, 0x1040, v106
	v_add3_u32 v82, 0, v82, v83
	v_add_u32_e32 v83, 0x10400, v82
	v_cmp_eq_u32_e64 s[6:7], 0, v103
	s_waitcnt vmcnt(5)
	v_mfma_f32_32x32x16_bf16 v[2:17], v[86:89], v[62:65], v[2:17]
	v_mfma_f32_32x32x16_bf16 v[18:33], v[86:89], v[58:61], v[18:33]
	s_waitcnt vmcnt(4)
	v_mfma_f32_32x32x16_bf16 v[2:17], v[90:93], v[50:53], v[2:17]
	v_mfma_f32_32x32x16_bf16 v[18:33], v[90:93], v[54:57], v[18:33]
	s_waitcnt vmcnt(3)
	v_mfma_f32_32x32x16_bf16 v[2:17], v[94:97], v[66:69], v[2:17]
	v_mfma_f32_32x32x16_bf16 v[18:33], v[94:97], v[70:73], v[18:33]
	s_waitcnt vmcnt(2)
	v_mfma_f32_32x32x16_bf16 v[2:17], v[156:159], v[74:77], v[2:17]
	v_mfma_f32_32x32x16_bf16 v[18:33], v[156:159], v[78:81], v[18:33]
	s_waitcnt vmcnt(1) lgkmcnt(1)
	v_mfma_f32_32x32x16_bf16 v[2:17], v[160:163], v[34:37], v[2:17]
	s_waitcnt lgkmcnt(0)
	v_mfma_f32_32x32x16_bf16 v[18:33], v[160:163], v[38:41], v[18:33]
	ds_read_b128 v[34:37], v0 offset:224
	ds_read_b128 v[38:41], v0 offset:8896
	s_waitcnt vmcnt(0) lgkmcnt(1)
	v_mfma_f32_32x32x16_bf16 v[2:17], v[164:167], v[34:37], v[2:17]
	s_waitcnt lgkmcnt(0)
	v_mfma_f32_32x32x16_bf16 v[18:33], v[164:167], v[38:41], v[18:33]
	global_load_dwordx4 v[34:37], v[98:99], off offset:384
	global_load_dwordx4 v[38:41], v[98:99], off offset:416
	global_load_dwordx4 v[42:45], v[98:99], off offset:448
	global_load_dwordx4 v[46:49], v[98:99], off offset:480
	s_nop 5
	v_mov_b32_e32 v50, v2
	s_nop 0
	v_mov_b32_e32 v51, v18
	v_mov_b32_e32 v18, v3
	s_waitcnt vmcnt(3)
	v_pk_add_f32 v[2:3], v[18:19], v[34:35] op_sel:[0,1]
	s_nop 0
	v_cvt_pk_bf16_f32 v67, v2, v3
	v_mov_b32_e32 v2, v4
	v_mov_b32_e32 v3, v20
	v_pk_add_f32 v[2:3], v[2:3], v[36:37] op_sel_hi:[1,0]
	v_mov_b32_e32 v20, v5
	v_mov_b32_e32 v0, v37
	v_cvt_pk_bf16_f32 v68, v2, v3
	v_pk_add_f32 v[2:3], v[20:21], v[0:1] op_sel_hi:[1,0]
	s_waitcnt vmcnt(2)
	v_mov_b32_e32 v0, v41
	v_cvt_pk_bf16_f32 v69, v2, v3
	v_mov_b32_e32 v2, v6
	v_mov_b32_e32 v3, v22
	v_pk_add_f32 v[2:3], v[2:3], v[38:39] op_sel_hi:[1,0]
	v_mov_b32_e32 v22, v7
	v_cvt_pk_bf16_f32 v70, v2, v3
	v_pk_add_f32 v[2:3], v[22:23], v[38:39] op_sel:[0,1]
	v_pk_add_f32 v[50:51], v[50:51], v[34:35] op_sel_hi:[1,0]
	v_cvt_pk_bf16_f32 v71, v2, v3
	v_mov_b32_e32 v2, v8
	v_mov_b32_e32 v3, v24
	v_pk_add_f32 v[2:3], v[2:3], v[40:41] op_sel_hi:[1,0]
	v_mov_b32_e32 v24, v9
	v_cvt_pk_bf16_f32 v72, v2, v3
	v_pk_add_f32 v[2:3], v[24:25], v[0:1] op_sel_hi:[1,0]
	s_waitcnt vmcnt(1)
	v_mov_b32_e32 v0, v45
	v_cvt_pk_bf16_f32 v73, v2, v3
	v_mov_b32_e32 v2, v10
	v_mov_b32_e32 v3, v26
	v_pk_add_f32 v[2:3], v[2:3], v[42:43] op_sel_hi:[1,0]
	v_mov_b32_e32 v26, v11
	v_cvt_pk_bf16_f32 v74, v2, v3
	v_pk_add_f32 v[2:3], v[26:27], v[42:43] op_sel:[0,1]
	v_cvt_pk_bf16_f32 v66, v50, v51
	v_cvt_pk_bf16_f32 v75, v2, v3
	v_mov_b32_e32 v2, v12
	v_mov_b32_e32 v3, v28
	v_pk_add_f32 v[2:3], v[2:3], v[44:45] op_sel_hi:[1,0]
	v_mov_b32_e32 v28, v13
	v_cvt_pk_bf16_f32 v76, v2, v3
	v_pk_add_f32 v[2:3], v[28:29], v[0:1] op_sel_hi:[1,0]
	s_waitcnt vmcnt(0)
	v_mov_b32_e32 v0, v49
	v_cvt_pk_bf16_f32 v77, v2, v3
	v_mov_b32_e32 v2, v14
	v_mov_b32_e32 v3, v30
	v_pk_add_f32 v[2:3], v[2:3], v[46:47] op_sel_hi:[1,0]
	v_mov_b32_e32 v30, v15
	v_cvt_pk_bf16_f32 v78, v2, v3
	v_pk_add_f32 v[2:3], v[30:31], v[46:47] op_sel:[0,1]
	s_nop 0
	v_cvt_pk_bf16_f32 v79, v2, v3
	v_mov_b32_e32 v2, v16
	v_mov_b32_e32 v3, v32
	v_pk_add_f32 v[2:3], v[2:3], v[48:49] op_sel_hi:[1,0]
	v_mov_b32_e32 v32, v17
	v_cvt_pk_bf16_f32 v80, v2, v3
	v_pk_add_f32 v[2:3], v[32:33], v[0:1] op_sel_hi:[1,0]
	v_lshlrev_b32_e32 v0, 4, v103
	v_cvt_pk_bf16_f32 v81, v2, v3
	v_lshl_add_u64 v[2:3], s[14:15], 0, v[0:1]
	v_lshl_add_u64 v[2:3], v[2:3], 0, s[4:5]
	v_add_co_u32_e32 v4, vcc, s74, v2
	s_movk_i32 s4, 0x2000
	s_nop 0
	v_addc_co_u32_e32 v5, vcc, 0, v3, vcc
	v_add_co_u32_e32 v6, vcc, s4, v2
	global_load_dwordx4 v[62:65], v[2:3], off
	global_load_dwordx4 v[58:61], v[2:3], off offset:2048
	v_addc_co_u32_e32 v7, vcc, 0, v3, vcc
	s_movk_i32 s4, 0x3000
	global_load_dwordx4 v[54:57], v[6:7], off offset:-4096
	global_load_dwordx4 v[50:53], v[4:5], off offset:2048
	global_load_dwordx4 v[46:49], v[6:7], off
	global_load_dwordx4 v[42:45], v[6:7], off offset:2048
	v_add_co_u32_e32 v4, vcc, s4, v2
	s_movk_i32 s4, 0x4000
	s_nop 0
	v_addc_co_u32_e32 v5, vcc, 0, v3, vcc
	v_add_co_u32_e32 v6, vcc, s4, v2
	s_movk_i32 s4, 0x5000
	s_nop 0
	v_addc_co_u32_e32 v7, vcc, 0, v3, vcc
	global_load_dwordx4 v[38:41], v[6:7], off offset:-4096
	global_load_dwordx4 v[34:37], v[4:5], off offset:2048
	global_load_dwordx4 v[30:33], v[6:7], off
	global_load_dwordx4 v[26:29], v[6:7], off offset:2048
	v_add_co_u32_e32 v4, vcc, s4, v2
	s_movk_i32 s4, 0x6000
	s_nop 0
	v_addc_co_u32_e32 v5, vcc, 0, v3, vcc
	v_add_co_u32_e32 v6, vcc, s4, v2
	s_movk_i32 s4, 0x7000
	s_nop 0
	v_addc_co_u32_e32 v7, vcc, 0, v3, vcc
	v_add_co_u32_e32 v2, vcc, s4, v2
	global_load_dwordx4 v[22:25], v[6:7], off offset:-4096
	global_load_dwordx4 v[18:21], v[4:5], off offset:2048
	global_load_dwordx4 v[14:17], v[6:7], off
	global_load_dwordx4 v[10:13], v[6:7], off offset:2048
	v_addc_co_u32_e32 v3, vcc, 0, v3, vcc
	global_load_dwordx4 v[6:9], v[2:3], off
	s_nop 0
	global_load_dwordx4 v[2:5], v[2:3], off offset:2048
	s_barrier
	ds_write_b16 v82, v107
	ds_write_b16_d16_hi v82, v107 offset:64
	ds_write_b16 v82, v108 offset:1040
	ds_write_b16_d16_hi v82, v108 offset:1104
	ds_write_b16 v82, v109 offset:2080
	ds_write_b16_d16_hi v82, v109 offset:2144
	ds_write_b16 v82, v110 offset:3120
	ds_write_b16_d16_hi v82, v110 offset:3184
	ds_write_b16 v82, v111 offset:8320
	ds_write_b16_d16_hi v82, v111 offset:8384
	ds_write_b16 v82, v112 offset:9360
	ds_write_b16_d16_hi v82, v112 offset:9424
	ds_write_b16 v82, v113 offset:10400
	ds_write_b16_d16_hi v82, v113 offset:10464
	ds_write_b16 v82, v114 offset:11440
	ds_write_b16_d16_hi v82, v114 offset:11504
	ds_write_b16 v82, v115 offset:16640
	ds_write_b16_d16_hi v82, v115 offset:16704
	ds_write_b16 v82, v116 offset:17680
	ds_write_b16_d16_hi v82, v116 offset:17744
	ds_write_b16 v82, v117 offset:18720
	ds_write_b16_d16_hi v82, v117 offset:18784
	ds_write_b16 v82, v118 offset:19760
	ds_write_b16_d16_hi v82, v118 offset:19824
	ds_write_b16 v82, v119 offset:24960
	ds_write_b16_d16_hi v82, v119 offset:25024
	ds_write_b16 v82, v120 offset:26000
	ds_write_b16_d16_hi v82, v120 offset:26064
	ds_write_b16 v82, v121 offset:27040
	ds_write_b16_d16_hi v82, v121 offset:27104
	ds_write_b16 v82, v122 offset:28080
	ds_write_b16_d16_hi v82, v122 offset:28144
	ds_write_b16 v82, v123 offset:33280
	ds_write_b16_d16_hi v82, v123 offset:33344
	ds_write_b16 v82, v124 offset:34320
	ds_write_b16_d16_hi v82, v124 offset:34384
	ds_write_b16 v82, v125 offset:35360
	ds_write_b16_d16_hi v82, v125 offset:35424
	ds_write_b16 v82, v126 offset:36400
	ds_write_b16_d16_hi v82, v126 offset:36464
	ds_write_b16 v82, v127 offset:41600
	ds_write_b16_d16_hi v82, v127 offset:41664
	ds_write_b16 v82, v128 offset:42640
	ds_write_b16_d16_hi v82, v128 offset:42704
	ds_write_b16 v82, v129 offset:43680
	ds_write_b16_d16_hi v82, v129 offset:43744
	ds_write_b16 v82, v130 offset:44720
	ds_write_b16_d16_hi v82, v130 offset:44784
	ds_write_b16 v82, v131 offset:49920
	ds_write_b16_d16_hi v82, v131 offset:49984
	ds_write_b16 v82, v132 offset:50960
	ds_write_b16_d16_hi v82, v132 offset:51024
	ds_write_b16 v82, v133 offset:52000
	ds_write_b16_d16_hi v82, v133 offset:52064
	ds_write_b16 v82, v134 offset:53040
	ds_write_b16_d16_hi v82, v134 offset:53104
	ds_write_b16 v82, v135 offset:58240
	ds_write_b16_d16_hi v82, v135 offset:58304
	ds_write_b16 v82, v136 offset:59280
	ds_write_b16_d16_hi v82, v136 offset:59344
	ds_write_b16 v82, v137 offset:60320
	ds_write_b16_d16_hi v82, v137 offset:60384
	ds_write_b16 v82, v138 offset:61360
	ds_write_b16_d16_hi v82, v138 offset:61424
	ds_write_b16 v83, v154
	v_add_u32_e32 v83, 0x10440, v82
	ds_write_b16_d16_hi v83, v154
	v_add_u32_e32 v83, 0x10810, v82
	ds_write_b16 v83, v150
	v_add_u32_e32 v83, 0x10850, v82
	ds_write_b16_d16_hi v83, v150
	v_add_u32_e32 v83, 0x10c20, v82
	ds_write_b16 v83, v151
	v_add_u32_e32 v83, 0x10c60, v82
	ds_write_b16_d16_hi v83, v151
	v_add_u32_e32 v83, 0x11030, v82
	ds_write_b16 v83, v152
	v_add_u32_e32 v83, 0x11070, v82
	ds_write_b16_d16_hi v83, v152
	v_add_u32_e32 v83, 0x12480, v82
	ds_write_b16 v83, v153
	v_add_u32_e32 v83, 0x124c0, v82
	ds_write_b16_d16_hi v83, v153
	v_add_u32_e32 v83, 0x12890, v82
	ds_write_b16 v83, v146
	v_add_u32_e32 v83, 0x128d0, v82
	ds_write_b16_d16_hi v83, v146
	v_add_u32_e32 v83, 0x12ca0, v82
	ds_write_b16 v83, v147
	v_add_u32_e32 v83, 0x12ce0, v82
	ds_write_b16_d16_hi v83, v147
	v_add_u32_e32 v83, 0x130b0, v82
	ds_write_b16 v83, v148
	v_add_u32_e32 v83, 0x130f0, v82
	ds_write_b16_d16_hi v83, v148
	v_add_u32_e32 v83, 0x14500, v82
	ds_write_b16 v83, v149
	v_add_u32_e32 v83, 0x14540, v82
	ds_write_b16_d16_hi v83, v149
	v_add_u32_e32 v83, 0x14910, v82
	ds_write_b16 v83, v142
	v_add_u32_e32 v83, 0x14950, v82
	ds_write_b16_d16_hi v83, v142
	v_add_u32_e32 v83, 0x14d20, v82
	ds_write_b16 v83, v143
	v_add_u32_e32 v83, 0x14d60, v82
	ds_write_b16_d16_hi v83, v143
	v_add_u32_e32 v83, 0x15130, v82
	ds_write_b16 v83, v144
	v_add_u32_e32 v83, 0x15170, v82
	ds_write_b16_d16_hi v83, v144
	v_add_u32_e32 v83, 0x16580, v82
	ds_write_b16 v83, v145
	v_add_u32_e32 v83, 0x165c0, v82
	ds_write_b16_d16_hi v83, v145
	v_add_u32_e32 v83, 0x16990, v82
	ds_write_b16 v83, v139
	v_add_u32_e32 v83, 0x169d0, v82
	ds_write_b16_d16_hi v83, v139
	v_add_u32_e32 v83, 0x16da0, v82
	ds_write_b16 v83, v140
	v_add_u32_e32 v83, 0x16de0, v82
	ds_write_b16_d16_hi v83, v140
	v_add_u32_e32 v83, 0x171b0, v82
	ds_write_b16 v83, v141
	v_add_u32_e32 v83, 0x171f0, v82
	ds_write_b16_d16_hi v83, v141
	v_add_u32_e32 v83, 0x18600, v82
	ds_write_b16 v83, v66
	v_add_u32_e32 v83, 0x18640, v82
	ds_write_b16_d16_hi v83, v66
	v_add_u32_e32 v66, 0x18a10, v82
	ds_write_b16 v66, v67
	v_add_u32_e32 v66, 0x18a50, v82
	ds_write_b16_d16_hi v66, v67
	v_add_u32_e32 v66, 0x18e20, v82
	ds_write_b16 v66, v68
	v_add_u32_e32 v66, 0x18e60, v82
	ds_write_b16_d16_hi v66, v68
	v_add_u32_e32 v66, 0x19230, v82
	ds_write_b16 v66, v69
	v_add_u32_e32 v66, 0x19270, v82
	ds_write_b16_d16_hi v66, v69
	v_add_u32_e32 v66, 0x1a680, v82
	ds_write_b16 v66, v70
	v_add_u32_e32 v66, 0x1a6c0, v82
	ds_write_b16_d16_hi v66, v70
	v_add_u32_e32 v66, 0x1aa90, v82
	ds_write_b16 v66, v71
	v_add_u32_e32 v66, 0x1aad0, v82
	ds_write_b16_d16_hi v66, v71
	v_add_u32_e32 v66, 0x1aea0, v82
	ds_write_b16 v66, v72
	v_add_u32_e32 v66, 0x1aee0, v82
	ds_write_b16_d16_hi v66, v72
	v_add_u32_e32 v66, 0x1b2b0, v82
	ds_write_b16 v66, v73
	v_add_u32_e32 v66, 0x1b2f0, v82
	ds_write_b16_d16_hi v66, v73
	v_add_u32_e32 v66, 0x1c700, v82
	ds_write_b16 v66, v74
	v_add_u32_e32 v66, 0x1c740, v82
	ds_write_b16_d16_hi v66, v74
	v_add_u32_e32 v66, 0x1cb10, v82
	ds_write_b16 v66, v75
	v_add_u32_e32 v66, 0x1cb50, v82
	ds_write_b16_d16_hi v66, v75
	v_add_u32_e32 v66, 0x1cf20, v82
	ds_write_b16 v66, v76
	v_add_u32_e32 v66, 0x1cf60, v82
	ds_write_b16_d16_hi v66, v76
	v_add_u32_e32 v66, 0x1d330, v82
	ds_write_b16 v66, v77
	v_add_u32_e32 v66, 0x1d370, v82
	ds_write_b16_d16_hi v66, v77
	v_add_u32_e32 v66, 0x1e780, v82
	ds_write_b16 v66, v78
	v_add_u32_e32 v66, 0x1e7c0, v82
	ds_write_b16_d16_hi v66, v78
	v_add_u32_e32 v66, 0x1eb90, v82
	ds_write_b16 v66, v79
	v_add_u32_e32 v66, 0x1ebd0, v82
	ds_write_b16_d16_hi v66, v79
	v_add_u32_e32 v66, 0x1efa0, v82
	v_add_u32_e32 v70, 0, v0
	v_xor_b32_e32 v0, 8, v234
	ds_write_b16 v66, v80
	v_add_u32_e32 v66, 0x1efe0, v82
	v_cmp_lt_i32_e32 vcc, v0, v104
	ds_write_b16_d16_hi v66, v80
	v_add_u32_e32 v66, 0x1f3b0, v82
	v_cndmask_b32_e32 v0, v234, v0, vcc
	s_mul_i32 s4, s12, 0x4100
	ds_write_b16 v66, v81
	v_add_u32_e32 v66, 0x1f3f0, v82
	v_lshlrev_b32_e32 v68, 2, v0
	v_xor_b32_e32 v0, 16, v234
	v_add_u32_e32 v69, s4, v70
	ds_write_b16_d16_hi v66, v81
	s_waitcnt lgkmcnt(0)
	s_barrier
	v_cmp_lt_i32_e32 vcc, v0, v104
	ds_read_b128 v[74:77], v69
	ds_read_b128 v[82:85], v69 offset:1040
	v_cndmask_b32_e32 v0, v234, v0, vcc
	v_lshlrev_b32_e32 v67, 2, v0
	v_xor_b32_e32 v0, 32, v234
	v_cmp_lt_i32_e32 vcc, v0, v104
	s_waitcnt vmcnt(15)
	v_lshlrev_b32_e32 v71, 16, v62
	v_and_b32_e32 v62, 0xffff0000, v62
	v_cndmask_b32_e32 v0, v234, v0, vcc
	v_lshlrev_b32_e32 v66, 2, v0
	s_waitcnt lgkmcnt(1)
	v_lshlrev_b32_e32 v0, 16, v74
	v_mul_f32_e32 v71, v71, v0
	v_and_b32_e32 v0, 0xffff0000, v74
	v_mul_f32_e32 v72, v62, v0
	v_lshlrev_b32_e32 v0, 16, v75
	v_lshlrev_b32_e32 v62, 16, v63
	v_mul_f32_e32 v73, v62, v0
	v_and_b32_e32 v0, 0xffff0000, v75
	v_and_b32_e32 v62, 0xffff0000, v63
	v_mul_f32_e32 v74, v62, v0
	v_lshlrev_b32_e32 v0, 16, v76
	v_lshlrev_b32_e32 v62, 16, v64
	v_mul_f32_e32 v62, v62, v0
	v_and_b32_e32 v0, 0xffff0000, v76
	v_and_b32_e32 v63, 0xffff0000, v64
	v_mul_f32_e32 v63, v63, v0
	v_lshlrev_b32_e32 v0, 16, v77
	v_lshlrev_b32_e32 v64, 16, v65
	v_mul_f32_e32 v64, v64, v0
	v_and_b32_e32 v0, 0xffff0000, v77
	v_and_b32_e32 v65, 0xffff0000, v65
	v_mul_f32_e32 v65, v65, v0
	s_waitcnt lgkmcnt(0)
	v_lshlrev_b32_e32 v0, 16, v82
	s_waitcnt vmcnt(14)
	v_lshlrev_b32_e32 v75, 16, v58
	v_mul_f32_e32 v79, v75, v0
	v_and_b32_e32 v0, 0xffff0000, v82
	v_and_b32_e32 v58, 0xffff0000, v58
	v_mul_f32_e32 v80, v58, v0
	v_lshlrev_b32_e32 v0, 16, v83
	v_lshlrev_b32_e32 v58, 16, v59
	v_mul_f32_e32 v81, v58, v0
	v_and_b32_e32 v0, 0xffff0000, v83
	v_and_b32_e32 v58, 0xffff0000, v59
	v_mul_f32_e32 v82, v58, v0
	v_lshlrev_b32_e32 v0, 16, v84
	v_lshlrev_b32_e32 v58, 16, v60
	v_mul_f32_e32 v75, v58, v0
	v_and_b32_e32 v0, 0xffff0000, v84
	v_and_b32_e32 v58, 0xffff0000, v60
	v_mul_f32_e32 v76, v58, v0
	v_lshlrev_b32_e32 v0, 16, v85
	v_lshlrev_b32_e32 v58, 16, v61
	v_mul_f32_e32 v77, v58, v0
	v_and_b32_e32 v0, 0xffff0000, v85
	ds_read_b128 v[84:87], v69 offset:2080
	ds_read_b128 v[90:93], v69 offset:3120
	v_and_b32_e32 v58, 0xffff0000, v61
	v_mul_f32_e32 v78, v58, v0
	s_waitcnt vmcnt(13)
	v_lshlrev_b32_e32 v58, 16, v54
	s_waitcnt lgkmcnt(1)
	v_lshlrev_b32_e32 v0, 16, v84
	v_mul_f32_e32 v58, v58, v0
	v_and_b32_e32 v0, 0xffff0000, v84
	v_and_b32_e32 v54, 0xffff0000, v54
	v_mul_f32_e32 v59, v54, v0
	v_lshlrev_b32_e32 v0, 16, v85
	v_lshlrev_b32_e32 v54, 16, v55
	v_mul_f32_e32 v60, v54, v0
	v_and_b32_e32 v0, 0xffff0000, v85
	v_and_b32_e32 v54, 0xffff0000, v55
	v_mul_f32_e32 v61, v54, v0
	v_lshlrev_b32_e32 v0, 16, v86
	v_lshlrev_b32_e32 v54, 16, v56
	v_mul_f32_e32 v54, v54, v0
	v_and_b32_e32 v0, 0xffff0000, v86
	v_and_b32_e32 v55, 0xffff0000, v56
	v_mul_f32_e32 v55, v55, v0
	v_lshlrev_b32_e32 v0, 16, v87
	v_lshlrev_b32_e32 v56, 16, v57
	v_mul_f32_e32 v56, v56, v0
	v_and_b32_e32 v0, 0xffff0000, v87
	v_and_b32_e32 v57, 0xffff0000, v57
	v_mul_f32_e32 v57, v57, v0
	s_waitcnt lgkmcnt(0)
	v_lshlrev_b32_e32 v0, 16, v90
	s_waitcnt vmcnt(12)
	v_lshlrev_b32_e32 v83, 16, v50
	v_mul_f32_e32 v87, v83, v0
	v_and_b32_e32 v0, 0xffff0000, v90
	v_and_b32_e32 v50, 0xffff0000, v50
	v_mul_f32_e32 v88, v50, v0
	v_lshlrev_b32_e32 v0, 16, v91
	v_lshlrev_b32_e32 v50, 16, v51
	v_mul_f32_e32 v89, v50, v0
	v_and_b32_e32 v0, 0xffff0000, v91
	v_and_b32_e32 v50, 0xffff0000, v51
	v_mul_f32_e32 v90, v50, v0
	v_lshlrev_b32_e32 v0, 16, v92
	v_lshlrev_b32_e32 v50, 16, v52
	v_mul_f32_e32 v83, v50, v0
	v_and_b32_e32 v0, 0xffff0000, v92
	v_and_b32_e32 v50, 0xffff0000, v52
	v_mul_f32_e32 v84, v50, v0
	v_lshlrev_b32_e32 v0, 16, v93
	v_lshlrev_b32_e32 v50, 16, v53
	v_mul_f32_e32 v85, v50, v0
	v_and_b32_e32 v0, 0xffff0000, v93
	ds_read_b128 v[92:95], v69 offset:4160
	ds_read_b128 v[104:107], v69 offset:5200
	v_and_b32_e32 v50, 0xffff0000, v53
	v_mul_f32_e32 v86, v50, v0
	s_waitcnt vmcnt(11)
	v_lshlrev_b32_e32 v50, 16, v46
	s_waitcnt lgkmcnt(1)
	v_lshlrev_b32_e32 v0, 16, v92
	v_mul_f32_e32 v50, v50, v0
	v_and_b32_e32 v0, 0xffff0000, v92
	v_and_b32_e32 v46, 0xffff0000, v46
	v_mul_f32_e32 v51, v46, v0
	v_lshlrev_b32_e32 v0, 16, v93
	v_lshlrev_b32_e32 v46, 16, v47
	v_mul_f32_e32 v52, v46, v0
	v_and_b32_e32 v0, 0xffff0000, v93
	v_and_b32_e32 v46, 0xffff0000, v47
	v_mul_f32_e32 v53, v46, v0
	v_lshlrev_b32_e32 v0, 16, v94
	v_lshlrev_b32_e32 v46, 16, v48
	v_mul_f32_e32 v46, v46, v0
	v_and_b32_e32 v0, 0xffff0000, v94
	v_and_b32_e32 v47, 0xffff0000, v48
	v_mul_f32_e32 v47, v47, v0
	v_lshlrev_b32_e32 v0, 16, v95
	v_lshlrev_b32_e32 v48, 16, v49
	v_mul_f32_e32 v48, v48, v0
	v_and_b32_e32 v0, 0xffff0000, v95
	v_and_b32_e32 v49, 0xffff0000, v49
	v_mul_f32_e32 v49, v49, v0
	s_waitcnt lgkmcnt(0)
	v_lshlrev_b32_e32 v0, 16, v104
	s_waitcnt vmcnt(10)
	v_lshlrev_b32_e32 v91, 16, v42
	v_mul_f32_e32 v95, v91, v0
	v_and_b32_e32 v0, 0xffff0000, v104
	v_and_b32_e32 v42, 0xffff0000, v42
	v_mul_f32_e32 v96, v42, v0
	v_lshlrev_b32_e32 v0, 16, v105
	v_lshlrev_b32_e32 v42, 16, v43
	v_mul_f32_e32 v97, v42, v0
	v_and_b32_e32 v0, 0xffff0000, v105
	v_and_b32_e32 v42, 0xffff0000, v43
	v_mul_f32_e32 v98, v42, v0
	v_lshlrev_b32_e32 v0, 16, v106
	v_lshlrev_b32_e32 v42, 16, v44
	v_mul_f32_e32 v91, v42, v0
	v_and_b32_e32 v0, 0xffff0000, v106
	v_and_b32_e32 v42, 0xffff0000, v44
	v_mul_f32_e32 v92, v42, v0
	v_lshlrev_b32_e32 v0, 16, v107
	v_lshlrev_b32_e32 v42, 16, v45
	v_mul_f32_e32 v93, v42, v0
	v_and_b32_e32 v0, 0xffff0000, v107
	ds_read_b128 v[104:107], v69 offset:6240
	ds_read_b128 v[108:111], v69 offset:7280
	v_and_b32_e32 v42, 0xffff0000, v45
	v_mul_f32_e32 v94, v42, v0
	s_waitcnt vmcnt(9)
	v_lshlrev_b32_e32 v42, 16, v38
	s_waitcnt lgkmcnt(1)
	v_lshlrev_b32_e32 v0, 16, v104
	v_mul_f32_e32 v42, v42, v0
	v_and_b32_e32 v0, 0xffff0000, v104
	v_and_b32_e32 v38, 0xffff0000, v38
	v_mul_f32_e32 v43, v38, v0
	v_lshlrev_b32_e32 v0, 16, v105
	v_lshlrev_b32_e32 v38, 16, v39
	v_mul_f32_e32 v44, v38, v0
	v_and_b32_e32 v0, 0xffff0000, v105
	v_and_b32_e32 v38, 0xffff0000, v39
	v_mul_f32_e32 v45, v38, v0
	v_lshlrev_b32_e32 v0, 16, v106
	v_lshlrev_b32_e32 v38, 16, v40
	v_mul_f32_e32 v38, v38, v0
	v_and_b32_e32 v0, 0xffff0000, v106
	v_and_b32_e32 v39, 0xffff0000, v40
	v_mul_f32_e32 v39, v39, v0
	v_lshlrev_b32_e32 v0, 16, v107
	v_lshlrev_b32_e32 v40, 16, v41
	v_mul_f32_e32 v40, v40, v0
	v_and_b32_e32 v0, 0xffff0000, v107
	v_and_b32_e32 v41, 0xffff0000, v41
	v_mul_f32_e32 v41, v41, v0
	s_waitcnt lgkmcnt(0)
	v_lshlrev_b32_e32 v0, 16, v108
	s_waitcnt vmcnt(8)
	v_lshlrev_b32_e32 v99, 16, v34
	v_mul_f32_e32 v105, v99, v0
	v_and_b32_e32 v0, 0xffff0000, v108
	v_and_b32_e32 v34, 0xffff0000, v34
	v_mul_f32_e32 v106, v34, v0
	v_lshlrev_b32_e32 v0, 16, v109
	v_lshlrev_b32_e32 v34, 16, v35
	v_mul_f32_e32 v107, v34, v0
	v_and_b32_e32 v0, 0xffff0000, v109
	v_and_b32_e32 v34, 0xffff0000, v35
	v_mul_f32_e32 v108, v34, v0
	v_lshlrev_b32_e32 v0, 16, v110
	v_lshlrev_b32_e32 v34, 16, v36
	v_mul_f32_e32 v99, v34, v0
	v_and_b32_e32 v0, 0xffff0000, v110
	v_and_b32_e32 v34, 0xffff0000, v36
	v_mul_f32_e32 v36, v34, v0
	v_lshlrev_b32_e32 v0, 16, v111
	v_lshlrev_b32_e32 v34, 16, v37
	v_mul_f32_e32 v104, v34, v0
	v_and_b32_e32 v0, 0xffff0000, v111
	v_and_b32_e32 v34, 0xffff0000, v37
	v_mul_f32_e32 v37, v34, v0
	v_max3_f32 v0, |v71|, 0, |v72|
	v_max3_f32 v0, v0, |v73|, |v74|
	v_max3_f32 v0, v0, |v62|, |v63|
	v_max3_f32 v0, v0, |v64|, |v65|
	s_nop 1
	v_max_f32_dpp v0, v0, v0 quad_perm:[1,0,3,2] row_mask:0xf bank_mask:0xf
	s_nop 1
	v_max_f32_dpp v0, v0, v0 quad_perm:[2,3,0,1] row_mask:0xf bank_mask:0xf
	s_nop 1
	v_max_f32_dpp v0, v0, v0 row_half_mirror row_mask:0xf bank_mask:0xf
	s_nop 1
	v_max_f32_dpp v0, v0, v0 row_ror:8 row_mask:0xf bank_mask:0xf
	v_mov_b32_e32 v114, v0
	s_nop 1
	v_permlane16_swap_b32_e32 v0, v114
	s_nop 0
	v_max_f32_e32 v0, v0, v114
	v_mov_b32_e32 v114, v0
	s_nop 1
	v_permlane32_swap_b32_e32 v0, v114
	s_nop 0
	v_max_f32_e32 v0, v0, v114
	v_mov_b32_e32 v114, v0
	v_max3_f32 v34, |v79|, 0, |v80|
	v_max3_f32 v34, v34, |v81|, |v82|
	v_max3_f32 v34, v34, |v75|, |v76|
	v_max3_f32 v34, v34, |v77|, |v78|
	s_waitcnt lgkmcnt(0)
	v_max_f32_e32 v114, v114, v114
	v_max_f32_e32 v0, v0, v114
	s_nop 1
	v_max_f32_dpp v34, v34, v34 quad_perm:[1,0,3,2] row_mask:0xf bank_mask:0xf
	s_nop 1
	v_max_f32_dpp v34, v34, v34 quad_perm:[2,3,0,1] row_mask:0xf bank_mask:0xf
	s_nop 1
	v_max_f32_dpp v34, v34, v34 row_half_mirror row_mask:0xf bank_mask:0xf
	s_nop 1
	v_max_f32_dpp v34, v34, v34 row_ror:8 row_mask:0xf bank_mask:0xf
	v_mov_b32_e32 v114, v34
	s_nop 1
	v_permlane16_swap_b32_e32 v34, v114
	s_nop 0
	v_max_f32_e32 v34, v34, v114
	v_mov_b32_e32 v114, v34
	s_nop 1
	v_permlane32_swap_b32_e32 v34, v114
	s_nop 0
	v_max_f32_e32 v34, v34, v114
	v_mov_b32_e32 v114, v34
	v_max3_f32 v35, |v58|, 0, |v59|
	v_max3_f32 v35, v35, |v60|, |v61|
	v_max3_f32 v35, v35, |v54|, |v55|
	v_max3_f32 v35, v35, |v56|, |v57|
	s_waitcnt lgkmcnt(0)
	v_max_f32_e32 v114, v114, v114
	v_max_f32_e32 v34, v34, v114
	s_nop 1
	v_max_f32_dpp v35, v35, v35 quad_perm:[1,0,3,2] row_mask:0xf bank_mask:0xf
	s_nop 1
	v_max_f32_dpp v35, v35, v35 quad_perm:[2,3,0,1] row_mask:0xf bank_mask:0xf
	s_nop 1
	v_max_f32_dpp v35, v35, v35 row_half_mirror row_mask:0xf bank_mask:0xf
	s_nop 1
	v_max_f32_dpp v35, v35, v35 row_ror:8 row_mask:0xf bank_mask:0xf
	v_mov_b32_e32 v114, v35
	s_nop 1
	v_permlane16_swap_b32_e32 v35, v114
	s_nop 0
	v_max_f32_e32 v35, v35, v114
	v_mov_b32_e32 v114, v35
	s_nop 1
	v_permlane32_swap_b32_e32 v35, v114
	s_nop 0
	v_max_f32_e32 v35, v35, v114
	v_mov_b32_e32 v114, v35
	v_max3_f32 v109, |v87|, 0, |v88|
	v_max3_f32 v109, v109, |v89|, |v90|
	v_max3_f32 v109, v109, |v83|, |v84|
	v_max3_f32 v109, v109, |v85|, |v86|
	s_waitcnt lgkmcnt(0)
	v_max_f32_e32 v114, v114, v114
	v_max_f32_e32 v35, v35, v114
	s_nop 1
	v_max_f32_dpp v109, v109, v109 quad_perm:[1,0,3,2] row_mask:0xf bank_mask:0xf
	s_nop 1
	v_max_f32_dpp v109, v109, v109 quad_perm:[2,3,0,1] row_mask:0xf bank_mask:0xf
	s_nop 1
	v_max_f32_dpp v109, v109, v109 row_half_mirror row_mask:0xf bank_mask:0xf
	s_nop 1
	v_max_f32_dpp v109, v109, v109 row_ror:8 row_mask:0xf bank_mask:0xf
	v_mov_b32_e32 v114, v109
	s_nop 1
	v_permlane16_swap_b32_e32 v109, v114
	s_nop 0
	v_max_f32_e32 v109, v109, v114
	v_mov_b32_e32 v114, v109
	s_nop 1
	v_permlane32_swap_b32_e32 v109, v114
	s_nop 0
	v_max_f32_e32 v109, v109, v114
	v_mov_b32_e32 v114, v109
	v_max3_f32 v110, |v50|, 0, |v51|
	v_max3_f32 v110, v110, |v52|, |v53|
	v_max3_f32 v110, v110, |v46|, |v47|
	v_max3_f32 v110, v110, |v48|, |v49|
	s_waitcnt lgkmcnt(0)
	v_max_f32_e32 v114, v114, v114
	v_max_f32_e32 v109, v109, v114
	s_nop 1
	v_max_f32_dpp v110, v110, v110 quad_perm:[1,0,3,2] row_mask:0xf bank_mask:0xf
	s_nop 1
	v_max_f32_dpp v110, v110, v110 quad_perm:[2,3,0,1] row_mask:0xf bank_mask:0xf
	s_nop 1
	v_max_f32_dpp v110, v110, v110 row_half_mirror row_mask:0xf bank_mask:0xf
	s_nop 1
	v_max_f32_dpp v110, v110, v110 row_ror:8 row_mask:0xf bank_mask:0xf
	v_mov_b32_e32 v114, v110
	s_nop 1
	v_permlane16_swap_b32_e32 v110, v114
	s_nop 0
	v_max_f32_e32 v110, v110, v114
	v_mov_b32_e32 v114, v110
	s_nop 1
	v_permlane32_swap_b32_e32 v110, v114
	s_nop 0
	v_max_f32_e32 v110, v110, v114
	v_mov_b32_e32 v114, v110
	v_max3_f32 v111, |v95|, 0, |v96|
	v_max3_f32 v111, v111, |v97|, |v98|
	v_max3_f32 v111, v111, |v91|, |v92|
	v_max3_f32 v111, v111, |v93|, |v94|
	s_waitcnt lgkmcnt(0)
	v_max_f32_e32 v114, v114, v114
	v_max_f32_e32 v110, v110, v114
	s_nop 1
	v_max_f32_dpp v111, v111, v111 quad_perm:[1,0,3,2] row_mask:0xf bank_mask:0xf
	s_nop 1
	v_max_f32_dpp v111, v111, v111 quad_perm:[2,3,0,1] row_mask:0xf bank_mask:0xf
	s_nop 1
	v_max_f32_dpp v111, v111, v111 row_half_mirror row_mask:0xf bank_mask:0xf
	s_nop 1
	v_max_f32_dpp v111, v111, v111 row_ror:8 row_mask:0xf bank_mask:0xf
	v_mov_b32_e32 v114, v111
	s_nop 1
	v_permlane16_swap_b32_e32 v111, v114
	s_nop 0
	v_max_f32_e32 v111, v111, v114
	v_mov_b32_e32 v114, v111
	s_nop 1
	v_permlane32_swap_b32_e32 v111, v114
	s_nop 0
	v_max_f32_e32 v111, v111, v114
	v_mov_b32_e32 v114, v111
	v_max3_f32 v112, |v42|, 0, |v43|
	v_max3_f32 v112, v112, |v44|, |v45|
	v_max3_f32 v112, v112, |v38|, |v39|
	v_max3_f32 v112, v112, |v40|, |v41|
	s_waitcnt lgkmcnt(0)
	v_max_f32_e32 v114, v114, v114
	v_max_f32_e32 v111, v111, v114
	s_nop 1
	v_max_f32_dpp v112, v112, v112 quad_perm:[1,0,3,2] row_mask:0xf bank_mask:0xf
	s_nop 1
	v_max_f32_dpp v112, v112, v112 quad_perm:[2,3,0,1] row_mask:0xf bank_mask:0xf
	s_nop 1
	v_max_f32_dpp v112, v112, v112 row_half_mirror row_mask:0xf bank_mask:0xf
	s_nop 1
	v_max_f32_dpp v112, v112, v112 row_ror:8 row_mask:0xf bank_mask:0xf
	v_mov_b32_e32 v114, v112
	s_nop 1
	v_permlane16_swap_b32_e32 v112, v114
	s_nop 0
	v_max_f32_e32 v112, v112, v114
	v_mov_b32_e32 v114, v112
	s_nop 1
	v_permlane32_swap_b32_e32 v112, v114
	s_nop 0
	v_max_f32_e32 v112, v112, v114
	v_mov_b32_e32 v114, v112
	v_max3_f32 v113, |v105|, 0, |v106|
	v_max3_f32 v113, v113, |v107|, |v108|
	v_max3_f32 v113, v113, |v99|, |v36|
	v_max3_f32 v113, v113, |v104|, |v37|
	s_waitcnt lgkmcnt(0)
	v_max_f32_e32 v114, v114, v114
	v_max_f32_e32 v112, v112, v114
	s_nop 1
	v_max_f32_dpp v113, v113, v113 quad_perm:[1,0,3,2] row_mask:0xf bank_mask:0xf
	s_nop 1
	v_max_f32_dpp v113, v113, v113 quad_perm:[2,3,0,1] row_mask:0xf bank_mask:0xf
	s_nop 1
	v_max_f32_dpp v113, v113, v113 row_half_mirror row_mask:0xf bank_mask:0xf
	s_nop 1
	v_max_f32_dpp v113, v113, v113 row_ror:8 row_mask:0xf bank_mask:0xf
	v_mov_b32_e32 v114, v113
	s_nop 1
	v_permlane16_swap_b32_e32 v113, v114
	s_nop 0
	v_max_f32_e32 v113, v113, v114
	v_mov_b32_e32 v114, v113
	s_nop 1
	v_permlane32_swap_b32_e32 v113, v114
	s_nop 0
	v_max_f32_e32 v113, v113, v114
	v_mov_b32_e32 v114, v113
	s_waitcnt lgkmcnt(0)
	v_max_f32_e32 v114, v114, v114
	v_max_f32_e32 v113, v113, v114
	v_mov_b32_e32 v114, v0
	s_waitcnt lgkmcnt(0)
	v_max_f32_e32 v114, v114, v114
	v_max_f32_e32 v0, v0, v114
	v_mov_b32_e32 v114, v34
	s_waitcnt lgkmcnt(0)
	v_max_f32_e32 v114, v114, v114
	v_max_f32_e32 v34, v34, v114
	v_mov_b32_e32 v114, v35
	s_waitcnt lgkmcnt(0)
	v_max_f32_e32 v114, v114, v114
	v_max_f32_e32 v35, v35, v114
	v_mov_b32_e32 v114, v109
	s_waitcnt lgkmcnt(0)
	v_max_f32_e32 v114, v114, v114
	v_max_f32_e32 v109, v109, v114
	v_mov_b32_e32 v114, v110
	s_waitcnt lgkmcnt(0)
	v_max_f32_e32 v114, v114, v114
	v_max_f32_e32 v110, v110, v114
	v_mov_b32_e32 v114, v111
	s_waitcnt lgkmcnt(0)
	v_max_f32_e32 v114, v114, v114
	v_max_f32_e32 v111, v111, v114
	v_mov_b32_e32 v114, v112
	s_waitcnt lgkmcnt(0)
	v_max_f32_e32 v114, v114, v114
	v_max_f32_e32 v112, v112, v114
	v_mov_b32_e32 v114, v113
	s_waitcnt lgkmcnt(0)
	v_max_f32_e32 v114, v114, v114
	v_max_f32_e32 v113, v113, v114
	v_mov_b32_e32 v114, v0
	s_waitcnt lgkmcnt(0)
	v_max_f32_e32 v114, v114, v114
	v_max_f32_e32 v0, v0, v114
	v_mov_b32_e32 v114, v34
	s_waitcnt lgkmcnt(0)
	v_max_f32_e32 v114, v114, v114
	v_max_f32_e32 v34, v34, v114
	v_mov_b32_e32 v114, v35
	s_waitcnt lgkmcnt(0)
	v_max_f32_e32 v114, v114, v114
	v_max_f32_e32 v35, v35, v114
	v_mov_b32_e32 v114, v109
	s_waitcnt lgkmcnt(0)
	v_max_f32_e32 v114, v114, v114
	v_max_f32_e32 v109, v109, v114
	v_mov_b32_e32 v114, v110
	s_waitcnt lgkmcnt(0)
	v_max_f32_e32 v114, v114, v114
	v_max_f32_e32 v110, v110, v114
	v_mov_b32_e32 v114, v111
	s_waitcnt lgkmcnt(0)
	v_max_f32_e32 v114, v114, v114
	v_max_f32_e32 v111, v111, v114
	v_mov_b32_e32 v114, v112
	s_waitcnt lgkmcnt(0)
	v_max_f32_e32 v114, v114, v114
	v_max_f32_e32 v112, v112, v114
	v_mov_b32_e32 v114, v113
	s_waitcnt lgkmcnt(0)
	v_max_f32_e32 v114, v114, v114
	v_max_f32_e32 v113, v113, v114
	v_mov_b32_e32 v114, v0
	s_waitcnt lgkmcnt(0)
	v_max_f32_e32 v114, v114, v114
	v_max_f32_e32 v0, v0, v114
	v_mov_b32_e32 v114, v34
	s_waitcnt lgkmcnt(0)
	v_max_f32_e32 v114, v114, v114
	v_max_f32_e32 v34, v34, v114
	v_mov_b32_e32 v114, v35
	s_waitcnt lgkmcnt(0)
	v_max_f32_e32 v114, v114, v114
	v_max_f32_e32 v35, v35, v114
	v_mov_b32_e32 v114, v109
	s_waitcnt lgkmcnt(0)
	v_max_f32_e32 v114, v114, v114
	v_max_f32_e32 v109, v109, v114
	v_mov_b32_e32 v114, v110
	s_waitcnt lgkmcnt(0)
	v_max_f32_e32 v114, v114, v114
	v_max_f32_e32 v110, v110, v114
	v_mov_b32_e32 v114, v111
	s_waitcnt lgkmcnt(0)
	v_max_f32_e32 v114, v114, v114
	v_max_f32_e32 v111, v111, v114
	v_mov_b32_e32 v114, v112
	s_waitcnt lgkmcnt(0)
	v_max_f32_e32 v114, v114, v114
	v_max_f32_e32 v112, v112, v114
	v_mov_b32_e32 v114, v113
	s_waitcnt lgkmcnt(0)
	v_max_f32_e32 v114, v114, v114
	v_max_f32_e32 v114, v113, v114
	v_mov_b32_e32 v113, v0
	s_waitcnt lgkmcnt(0)
	v_max_f32_e32 v113, v113, v113
	v_max_f32_e32 v0, v0, v113
	v_mov_b32_e32 v113, v34
	s_waitcnt lgkmcnt(0)
	v_max_f32_e32 v113, v113, v113
	v_max_f32_e32 v120, v34, v113
	v_mov_b32_e32 v34, v35
	v_mov_b32_e32 v122, v120
	s_waitcnt lgkmcnt(0)
	v_max_f32_e32 v34, v34, v34
	v_max_f32_e32 v118, v35, v34
	v_mov_b32_e32 v34, v109
	v_mov_b32_e32 v121, v118
	s_waitcnt lgkmcnt(0)
	v_max_f32_e32 v34, v34, v34
	v_max_f32_e32 v116, v109, v34
	v_mov_b32_e32 v34, v110
	v_mov_b32_e32 v119, v116
	s_waitcnt lgkmcnt(0)
	v_max_f32_e32 v34, v34, v34
	v_max_f32_e32 v115, v110, v34
	v_mov_b32_e32 v34, v111
	v_mov_b32_e32 v117, v115
	s_waitcnt lgkmcnt(0)
	v_max_f32_e32 v34, v34, v34
	v_max_f32_e32 v113, v111, v34
	v_mov_b32_e32 v34, v112
	s_waitcnt lgkmcnt(0)
	v_max_f32_e32 v34, v34, v34
	v_max_f32_e32 v111, v112, v34
	v_mov_b32_e32 v34, v114
	v_mov_b32_e32 v112, v111
	s_waitcnt lgkmcnt(0)
	v_max_f32_e32 v34, v34, v34
	v_max_f32_e32 v109, v114, v34
	v_mov_b32_e32 v34, v0
	v_mov_b32_e32 v114, v113
	v_mov_b32_e32 v110, v109
	s_waitcnt lgkmcnt(0)
	v_max3_f32 v123, v0, v34, s72
	s_and_saveexec_b64 s[12:13], s[6:7]
	s_cbranch_execz .LBB0_490
	s_lshl_b64 s[4:5], s[16:17], 2
	s_add_u32 s4, s18, s4
	s_addc_u32 s5, s19, s5
	v_mul_f32_e32 v0, 0x3c010204, v123
	global_store_dword v1, v0, s[4:5]
